# norm2+router: router weight fragments issued at the top of each row block, h stores moved behind the MFMA section
# speedup vs baseline: 1.0025x; 1.0025x over previous
; template <int MODE>
; __device__ __forceinline__ void norm_phase(const MkArgs& a, LAS unsigned char* lds, const int l, const int wv) {
;     ...
;         float xv[64];
; #pragma unroll
;         for (int j = 0; j < 8; ++j) {
;             const int k = 256 * w + 32 * j + 8 * q;
;             const f32x4 v0 = *(const f32x4*)(xsrc + (size_t)t * DM + k), v1 = *(const f32x4*)(xsrc + (size_t)t * DM + k + 4);
;             xv[8 * j + 0] = v0[0]; xv[8 * j + 1] = v0[1]; xv[8 * j + 2] = v0[2]; xv[8 * j + 3] = v0[3];
;             xv[8 * j + 4] = v1[0]; xv[8 * j + 5] = v1[1]; xv[8 * j + 6] = v1[2]; xv[8 * j + 7] = v1[3];
;         }
;     ...
;         float ss = 0.f;
; #pragma unroll
;         for (int i = 0; i < 64; ++i) ss += xv[i] * xv[i];
;         ss += __shfl_xor(ss, 16); ss += __shfl_xor(ss, 32);
;         if (q == 0) ssp[w * 16 + r] = ss;
.LBB0_899:
	s_lshl_b32 s30, s29, 4
	v_or_b32_e32 v82, s30, v148
	v_ashrrev_i32_e32 v83, 31, v82
	v_lshlrev_b64 v[0:1], 13, v[82:83]
	v_lshl_add_u64 v[0:1], v[68:69], 0, v[0:1]
	global_load_dwordx4 v[60:63], v[0:1], off
	global_load_dwordx4 v[44:47], v[0:1], off offset:16
	global_load_dwordx4 v[56:59], v[0:1], off offset:128
	global_load_dwordx4 v[24:27], v[0:1], off offset:144
	global_load_dwordx4 v[52:55], v[0:1], off offset:256
	global_load_dwordx4 v[4:7], v[0:1], off offset:272
	global_load_dwordx4 v[48:51], v[0:1], off offset:384
	global_load_dwordx4 v[8:11], v[0:1], off offset:400
	global_load_dwordx4 v[40:43], v[0:1], off offset:512
	global_load_dwordx4 v[12:15], v[0:1], off offset:528
	global_load_dwordx4 v[36:39], v[0:1], off offset:640
	global_load_dwordx4 v[16:19], v[0:1], off offset:656
	global_load_dwordx4 v[32:35], v[0:1], off offset:768
	global_load_dwordx4 v[20:23], v[0:1], off offset:784
	global_load_dwordx4 v[28:31], v[0:1], off offset:896
	s_nop 0
	global_load_dwordx4 v[0:3], v[0:1], off offset:912
	global_load_dwordx4 v[186:189], v152, s[22:23]
	global_load_dwordx4 v[190:193], v152, s[22:23] offset:1024
	global_load_dwordx4 v[194:197], v152, s[22:23] offset:2048
	global_load_dwordx4 v[198:201], v152, s[22:23] offset:3072
	s_add_u32 s100, s22, 0x1000
	s_addc_u32 s101, s23, 0
	global_load_dwordx4 v[202:205], v152, s[100:101]
	global_load_dwordx4 v[206:209], v152, s[100:101] offset:1024
	global_load_dwordx4 v[210:213], v152, s[100:101] offset:2048
	global_load_dwordx4 v[214:217], v152, s[100:101] offset:3072
	s_add_u32 s100, s22, 0x2000
	s_addc_u32 s101, s23, 0
	global_load_dwordx4 v[218:221], v152, s[100:101]
	global_load_dwordx4 v[222:225], v152, s[100:101] offset:1024
	global_load_dwordx4 v[226:229], v152, s[100:101] offset:2048
	global_load_dwordx4 v[230:233], v152, s[100:101] offset:3072
	s_add_u32 s100, s22, 0x3000
	s_addc_u32 s101, s23, 0
	global_load_dwordx4 v[234:237], v152, s[100:101]
	global_load_dwordx4 v[238:241], v152, s[100:101] offset:1024
	global_load_dwordx4 v[242:245], v152, s[100:101] offset:2048
	global_load_dwordx4 v[246:249], v152, s[100:101] offset:3072
	s_waitcnt vmcnt(31)
	v_mul_f32_e32 v76, v61, v61
	v_fmac_f32_e32 v76, v60, v60
	v_fmac_f32_e32 v76, v62, v62
	v_fmac_f32_e32 v76, v63, v63
	s_waitcnt vmcnt(30)
	v_fmac_f32_e32 v76, v44, v44
	v_fmac_f32_e32 v76, v45, v45
	v_fmac_f32_e32 v76, v46, v46
	v_fmac_f32_e32 v76, v47, v47
	s_waitcnt vmcnt(29)
	v_fmac_f32_e32 v76, v56, v56
	v_fmac_f32_e32 v76, v57, v57
	v_fmac_f32_e32 v76, v58, v58
	v_fmac_f32_e32 v76, v59, v59
	s_waitcnt vmcnt(28)
	v_fmac_f32_e32 v76, v24, v24
	v_fmac_f32_e32 v76, v25, v25
	v_fmac_f32_e32 v76, v26, v26
	v_fmac_f32_e32 v76, v27, v27
	s_waitcnt vmcnt(27)
	v_fmac_f32_e32 v76, v52, v52
	v_fmac_f32_e32 v76, v53, v53
	v_fmac_f32_e32 v76, v54, v54
	v_fmac_f32_e32 v76, v55, v55
	s_waitcnt vmcnt(26)
	v_fmac_f32_e32 v76, v4, v4
	v_fmac_f32_e32 v76, v5, v5
	v_fmac_f32_e32 v76, v6, v6
	v_fmac_f32_e32 v76, v7, v7
	s_waitcnt vmcnt(25)
	v_fmac_f32_e32 v76, v48, v48
	v_fmac_f32_e32 v76, v49, v49
	v_fmac_f32_e32 v76, v50, v50
	v_fmac_f32_e32 v76, v51, v51
	s_waitcnt vmcnt(24)
	v_fmac_f32_e32 v76, v8, v8
	v_fmac_f32_e32 v76, v9, v9
	v_fmac_f32_e32 v76, v10, v10
	v_fmac_f32_e32 v76, v11, v11
	s_waitcnt vmcnt(23)
	v_fmac_f32_e32 v76, v40, v40
	v_fmac_f32_e32 v76, v41, v41
	v_fmac_f32_e32 v76, v42, v42
	v_fmac_f32_e32 v76, v43, v43
	s_waitcnt vmcnt(22)
	v_fmac_f32_e32 v76, v12, v12
	v_fmac_f32_e32 v76, v13, v13
	v_fmac_f32_e32 v76, v14, v14
	v_fmac_f32_e32 v76, v15, v15
	s_waitcnt vmcnt(21)
	v_fmac_f32_e32 v76, v36, v36
	v_fmac_f32_e32 v76, v37, v37
	v_fmac_f32_e32 v76, v38, v38
	v_fmac_f32_e32 v76, v39, v39
	s_waitcnt vmcnt(20)
	v_fmac_f32_e32 v76, v16, v16
	v_fmac_f32_e32 v76, v17, v17
	v_fmac_f32_e32 v76, v18, v18
	v_fmac_f32_e32 v76, v19, v19
	s_waitcnt vmcnt(19)
	v_fmac_f32_e32 v76, v32, v32
	v_fmac_f32_e32 v76, v33, v33
	v_fmac_f32_e32 v76, v34, v34
	v_fmac_f32_e32 v76, v35, v35
	s_waitcnt vmcnt(18)
	v_fmac_f32_e32 v76, v20, v20
	v_fmac_f32_e32 v76, v21, v21
	v_fmac_f32_e32 v76, v22, v22
	v_fmac_f32_e32 v76, v23, v23
	s_waitcnt vmcnt(17)
	v_fmac_f32_e32 v76, v28, v28
	v_fmac_f32_e32 v76, v29, v29
	v_fmac_f32_e32 v76, v30, v30
	v_fmac_f32_e32 v76, v31, v31
	s_waitcnt vmcnt(16)
	v_fmac_f32_e32 v76, v0, v0
	v_fmac_f32_e32 v76, v1, v1
	v_fmac_f32_e32 v76, v2, v2
	v_fmac_f32_e32 v76, v3, v3
	ds_bpermute_b32 v84, v149, v76
	s_waitcnt lgkmcnt(0)
	v_add_f32_e32 v76, v76, v84
	ds_bpermute_b32 v84, v150, v76
	s_and_saveexec_b64 s[12:13], s[8:9]
	s_cbranch_execz .LBB0_901
	v_readlane_b32 s14, v252, 39
	s_waitcnt lgkmcnt(0)
	v_add_f32_e32 v76, v76, v84
	v_add_u32_e32 v84, s14, v151
	ds_write_b32 v84, v76
; #define LAS __attribute__((address_space(3)))
; __device__ __forceinline__ unsigned cvt_pk_bf16(float lo, float hi) { const bf16x2_t r = __builtin_convertvector((f32x2_t){lo, hi}, bf16x2_t); return __builtin_bit_cast(unsigned, r); }
; template <int MODE>
; __device__ __forceinline__ void norm_phase(const MkArgs& a, LAS unsigned char* lds, const int l, const int wv) {
;     ...
;         float tot = 0.f;
; #pragma unroll
;         for (int i = 0; i < 8; ++i) tot += ssp[i * 16 + r];
;         const float rstd = 1.0f / sqrtf(tot * (1.0f / DM) + EPSV);
; #pragma unroll
;         for (int j = 0; j < 8; ++j) {
;             const int k = 256 * w + 32 * j + 8 * q;
;             const f32x4 g0 = *(const LAS f32x4*)&tabA[k], g1 = *(const LAS f32x4*)&tabA[k + 4];
;             float gg[8] = {g0[0], g0[1], g0[2], g0[3], g1[0], g1[1], g1[2], g1[3]};
;             if constexpr (MODE != 3) {
;                 const f32x4 s0 = *(const LAS f32x4*)&tabB[k], s1 = *(const LAS f32x4*)&tabB[k + 4];
;                 const float sv[8] = {s0[0], s0[1], s0[2], s0[3], s1[0], s1[1], s1[2], s1[3]};
; #pragma unroll
;                 for (int i = 0; i < 8; ++i) xv[8 * j + i] = (xv[8 * j + i] * rstd) * gg[i] + sv[i];
;                 u32x4 o; o[0] = cvt_pk_bf16(xv[8 * j + 0], xv[8 * j + 1]); o[1] = cvt_pk_bf16(xv[8 * j + 2], xv[8 * j + 3]);
;                 o[2] = cvt_pk_bf16(xv[8 * j + 4], xv[8 * j + 5]); o[3] = cvt_pk_bf16(xv[8 * j + 6], xv[8 * j + 7]);
;                 *(u32x4*)(hb + (size_t)t * DM + k) = o;
.LBB0_901:
	s_or_b64 exec, exec, s[12:13]
	s_waitcnt lgkmcnt(0)
	s_barrier
	ds_read2_b32 v[84:85], v151 offset1:16
	ds_read2_b32 v[86:87], v151 offset0:32 offset1:48
	ds_read2_b32 v[88:89], v151 offset0:64 offset1:80
	s_mov_b32 s12, 0xf800000
	v_lshlrev_b64 v[82:83], 12, v[82:83]
	s_waitcnt lgkmcnt(2)
	v_add_f32_e32 v76, 0, v84
	v_add_f32_e32 v76, v76, v85
	ds_read2_b32 v[84:85], v151 offset0:96 offset1:112
	s_waitcnt lgkmcnt(2)
	v_add_f32_e32 v76, v76, v86
	v_add_f32_e32 v76, v76, v87
	s_waitcnt lgkmcnt(1)
	v_add_f32_e32 v76, v76, v88
	v_add_f32_e32 v76, v76, v89
	s_waitcnt lgkmcnt(0)
	v_add_f32_e32 v76, v76, v84
	v_add_f32_e32 v76, v76, v85
	v_fmamk_f32 v76, v76, 0x3a000000, v154
	v_mul_f32_e32 v84, 0x4f800000, v76
	v_cmp_gt_f32_e32 vcc, s12, v76
	v_lshl_add_u64 v[172:173], v[70:71], 0, v[82:83]
	s_nop 0
	v_cndmask_b32_e32 v76, v76, v84, vcc
	v_sqrt_f32_e32 v84, v76
	s_nop 0
	v_add_u32_e32 v85, -1, v84
	v_fma_f32 v86, -v85, v84, v76
	v_cmp_ge_f32_e64 s[12:13], 0, v86
	v_add_u32_e32 v86, 1, v84
	s_nop 0
	v_cndmask_b32_e64 v85, v84, v85, s[12:13]
	v_fma_f32 v84, -v86, v84, v76
	v_cmp_lt_f32_e64 s[12:13], 0, v84
	s_nop 1
	v_cndmask_b32_e64 v84, v85, v86, s[12:13]
	v_mul_f32_e32 v85, 0x37800000, v84
	v_cndmask_b32_e32 v84, v84, v85, vcc
	v_cmp_class_f32_e32 vcc, v76, v155
	s_nop 1
	v_cndmask_b32_e32 v76, v84, v76, vcc
	v_div_scale_f32 v84, s[12:13], v76, v76, 1.0
	v_rcp_f32_e32 v85, v84
	s_movk_i32 s12, 0x2000
	v_fma_f32 v86, -v84, v85, 1.0
	v_fmac_f32_e32 v85, v86, v85
	v_div_scale_f32 v86, vcc, 1.0, v76, 1.0
	v_mul_f32_e32 v87, v86, v85
	v_fma_f32 v88, -v84, v87, v86
	v_fmac_f32_e32 v87, v88, v85
	v_fma_f32 v84, -v84, v87, v86
	v_div_fmas_f32 v84, v84, v85, v87
	v_div_fixup_f32 v76, v84, v76, 1.0
	ds_read_b128 v[84:87], v65
	ds_read_b128 v[88:91], v118
	ds_read_b128 v[92:95], v117
	ds_read_b128 v[96:99], v119
	v_pk_mul_f32 v[60:61], v[60:61], v[76:77] op_sel_hi:[1,0]
	v_pk_mul_f32 v[44:45], v[44:45], v[76:77] op_sel_hi:[1,0]
	v_pk_mul_f32 v[56:57], v[56:57], v[76:77] op_sel_hi:[1,0]
	s_waitcnt lgkmcnt(2)
	v_pk_fma_f32 v[108:109], v[84:85], v[60:61], v[88:89]
	v_pk_mul_f32 v[60:61], v[62:63], v[76:77] op_sel_hi:[1,0]
	s_waitcnt lgkmcnt(0)
	v_pk_fma_f32 v[106:107], v[92:93], v[44:45], v[96:97]
	v_pk_mul_f32 v[44:45], v[46:47], v[76:77] op_sel_hi:[1,0]
	v_pk_fma_f32 v[112:113], v[86:87], v[60:61], v[90:91]
	v_pk_fma_f32 v[110:111], v[94:95], v[44:45], v[98:99]
	v_cvt_pk_bf16_f32 v44, v108, v109
	v_cvt_pk_bf16_f32 v45, v112, v113
	v_cvt_pk_bf16_f32 v46, v106, v107
	v_cvt_pk_bf16_f32 v47, v110, v111
	ds_read_b128 v[60:63], v120
	ds_read_b128 v[82:85], v122
	ds_read_b128 v[86:89], v121
	ds_read_b128 v[90:93], v123
	v_pk_mul_f32 v[24:25], v[24:25], v[76:77] op_sel_hi:[1,0]
	v_pk_mul_f32 v[52:53], v[52:53], v[76:77] op_sel_hi:[1,0]
	s_waitcnt lgkmcnt(2)
	v_pk_fma_f32 v[98:99], v[56:57], v[60:61], v[82:83]
	v_pk_mul_f32 v[56:57], v[58:59], v[76:77] op_sel_hi:[1,0]
	s_waitcnt lgkmcnt(0)
	v_pk_fma_f32 v[100:101], v[24:25], v[86:87], v[90:91]
	v_pk_mul_f32 v[24:25], v[26:27], v[76:77] op_sel_hi:[1,0]
	v_pk_fma_f32 v[102:103], v[56:57], v[62:63], v[84:85]
	v_pk_fma_f32 v[104:105], v[24:25], v[88:89], v[92:93]
	v_cvt_pk_bf16_f32 v24, v98, v99
	v_cvt_pk_bf16_f32 v25, v102, v103
	v_cvt_pk_bf16_f32 v26, v100, v101
	v_cvt_pk_bf16_f32 v27, v104, v105
	ds_read_b128 v[56:59], v124
	ds_read_b128 v[60:63], v126
	ds_read_b128 v[82:85], v125
	ds_read_b128 v[86:89], v127
	v_pk_mul_f32 v[4:5], v[4:5], v[76:77] op_sel_hi:[1,0]
	v_pk_mul_f32 v[48:49], v[48:49], v[76:77] op_sel_hi:[1,0]
	s_waitcnt lgkmcnt(2)
	v_pk_fma_f32 v[90:91], v[52:53], v[56:57], v[60:61]
	v_pk_mul_f32 v[52:53], v[54:55], v[76:77] op_sel_hi:[1,0]
	s_waitcnt lgkmcnt(0)
	v_pk_fma_f32 v[92:93], v[4:5], v[82:83], v[86:87]
	v_pk_mul_f32 v[4:5], v[6:7], v[76:77] op_sel_hi:[1,0]
	v_pk_fma_f32 v[94:95], v[52:53], v[58:59], v[62:63]
	v_pk_fma_f32 v[96:97], v[4:5], v[84:85], v[88:89]
	v_cvt_pk_bf16_f32 v4, v90, v91
	v_cvt_pk_bf16_f32 v5, v94, v95
	v_cvt_pk_bf16_f32 v6, v92, v93
	v_cvt_pk_bf16_f32 v7, v96, v97
	ds_read_b128 v[52:55], v128
	ds_read_b128 v[56:59], v130
	ds_read_b128 v[60:63], v129
	ds_read_b128 v[82:85], v131
	v_pk_mul_f32 v[50:51], v[50:51], v[76:77] op_sel_hi:[1,0]
	v_pk_mul_f32 v[8:9], v[8:9], v[76:77] op_sel_hi:[1,0]
	s_waitcnt lgkmcnt(2)
	v_pk_fma_f32 v[48:49], v[48:49], v[52:53], v[56:57]
	v_pk_fma_f32 v[52:53], v[50:51], v[54:55], v[58:59]
	s_waitcnt lgkmcnt(0)
	v_pk_fma_f32 v[50:51], v[8:9], v[60:61], v[82:83]
	v_pk_mul_f32 v[8:9], v[10:11], v[76:77] op_sel_hi:[1,0]
	v_cvt_pk_bf16_f32 v10, v50, v51
	v_pk_fma_f32 v[54:55], v[8:9], v[62:63], v[84:85]
	v_cvt_pk_bf16_f32 v8, v48, v49
	v_cvt_pk_bf16_f32 v9, v52, v53
	v_cvt_pk_bf16_f32 v11, v54, v55
	ds_read_b128 v[56:59], v132
	ds_read_b128 v[60:63], v134
	ds_read_b128 v[82:85], v133
	ds_read_b128 v[86:89], v135
	v_pk_mul_f32 v[40:41], v[40:41], v[76:77] op_sel_hi:[1,0]
	v_pk_mul_f32 v[42:43], v[42:43], v[76:77] op_sel_hi:[1,0]
	v_pk_mul_f32 v[12:13], v[12:13], v[76:77] op_sel_hi:[1,0]
	s_waitcnt lgkmcnt(2)
	v_pk_fma_f32 v[40:41], v[40:41], v[56:57], v[60:61]
	v_pk_fma_f32 v[56:57], v[42:43], v[58:59], v[62:63]
	s_waitcnt lgkmcnt(0)
	v_pk_fma_f32 v[42:43], v[12:13], v[82:83], v[86:87]
	v_pk_mul_f32 v[12:13], v[14:15], v[76:77] op_sel_hi:[1,0]
	v_cvt_pk_bf16_f32 v14, v42, v43
	v_pk_fma_f32 v[58:59], v[12:13], v[84:85], v[88:89]
	v_cvt_pk_bf16_f32 v12, v40, v41
	v_cvt_pk_bf16_f32 v13, v56, v57
	v_cvt_pk_bf16_f32 v15, v58, v59
	ds_read_b128 v[60:63], v136
	ds_read_b128 v[82:85], v138
	ds_read_b128 v[86:89], v137
	ds_read_b128 v[160:163], v139
	v_pk_mul_f32 v[36:37], v[36:37], v[76:77] op_sel_hi:[1,0]
	v_pk_mul_f32 v[38:39], v[38:39], v[76:77] op_sel_hi:[1,0]
	v_pk_mul_f32 v[16:17], v[16:17], v[76:77] op_sel_hi:[1,0]
	s_waitcnt lgkmcnt(2)
; __device__ __forceinline__ unsigned cvt_pk_bf16(float lo, float hi) { const bf16x2_t r = __builtin_convertvector((f32x2_t){lo, hi}, bf16x2_t); return __builtin_bit_cast(unsigned, r); }
; #define RT_LOAD(fr, c) do { _Pragma("unroll") for (int i = 0; i < 16; ++i) fr[i] = WFRAG((c) * 16 + i); } while (0)
; template <int MODE>
; __device__ __forceinline__ void norm_phase(const MkArgs& a, LAS unsigned char* lds, const int l, const int wv) {
;     ...
;                 for (int i = 0; i < 8; ++i) xv[8 * j + i] = (xv[8 * j + i] * rstd) * gg[i] + sv[i];
;                 u32x4 o; o[0] = cvt_pk_bf16(xv[8 * j + 0], xv[8 * j + 1]); o[1] = cvt_pk_bf16(xv[8 * j + 2], xv[8 * j + 3]);
;                 o[2] = cvt_pk_bf16(xv[8 * j + 4], xv[8 * j + 5]); o[3] = cvt_pk_bf16(xv[8 * j + 6], xv[8 * j + 7]);
;                 *(u32x4*)(hb + (size_t)t * DM + k) = o;
;     ...
;             u32x4 frA[16], frB[16];
;     ...
;             RT_LOAD(frA, 0); RT_LOAD(frB, 1);
;             RT_MMA(frA, 0);
;             RT_LOAD(frA, 2);
;             RT_MMA(frB, 1);
;             RT_MMA(frA, 2);
	v_pk_fma_f32 v[36:37], v[36:37], v[60:61], v[82:83]
	v_pk_fma_f32 v[60:61], v[38:39], v[62:63], v[84:85]
	s_waitcnt lgkmcnt(0)
	v_pk_fma_f32 v[38:39], v[16:17], v[86:87], v[160:161]
	v_pk_mul_f32 v[16:17], v[18:19], v[76:77] op_sel_hi:[1,0]
	v_cvt_pk_bf16_f32 v18, v38, v39
	v_pk_fma_f32 v[62:63], v[16:17], v[88:89], v[162:163]
	v_cvt_pk_bf16_f32 v16, v36, v37
	v_cvt_pk_bf16_f32 v17, v60, v61
	v_cvt_pk_bf16_f32 v19, v62, v63
	ds_read_b128 v[82:85], v140
	ds_read_b128 v[86:89], v142
	ds_read_b128 v[160:163], v141
	ds_read_b128 v[164:167], v143
	v_pk_mul_f32 v[32:33], v[32:33], v[76:77] op_sel_hi:[1,0]
	v_pk_mul_f32 v[34:35], v[34:35], v[76:77] op_sel_hi:[1,0]
	v_pk_mul_f32 v[20:21], v[20:21], v[76:77] op_sel_hi:[1,0]
	s_waitcnt lgkmcnt(2)
	v_pk_fma_f32 v[32:33], v[32:33], v[82:83], v[86:87]
	v_pk_fma_f32 v[82:83], v[34:35], v[84:85], v[88:89]
	s_waitcnt lgkmcnt(0)
	v_pk_fma_f32 v[34:35], v[20:21], v[160:161], v[164:165]
	v_pk_mul_f32 v[20:21], v[22:23], v[76:77] op_sel_hi:[1,0]
	v_cvt_pk_bf16_f32 v22, v34, v35
	v_pk_fma_f32 v[84:85], v[20:21], v[162:163], v[166:167]
	v_cvt_pk_bf16_f32 v20, v32, v33
	v_cvt_pk_bf16_f32 v21, v82, v83
	v_cvt_pk_bf16_f32 v23, v84, v85
	ds_read_b128 v[86:89], v144
	ds_read_b128 v[160:163], v146
	ds_read_b128 v[164:167], v145
	ds_read_b128 v[168:171], v147
	v_pk_mul_f32 v[28:29], v[28:29], v[76:77] op_sel_hi:[1,0]
	v_pk_mul_f32 v[30:31], v[30:31], v[76:77] op_sel_hi:[1,0]
	v_pk_mul_f32 v[0:1], v[0:1], v[76:77] op_sel_hi:[1,0]
	s_waitcnt lgkmcnt(2)
	v_pk_fma_f32 v[28:29], v[28:29], v[86:87], v[160:161]
	v_pk_fma_f32 v[86:87], v[30:31], v[88:89], v[162:163]
	s_waitcnt lgkmcnt(0)
	v_pk_fma_f32 v[30:31], v[0:1], v[164:165], v[168:169]
	v_pk_mul_f32 v[0:1], v[2:3], v[76:77] op_sel_hi:[1,0]
	v_cvt_pk_bf16_f32 v2, v30, v31
	v_pk_fma_f32 v[88:89], v[0:1], v[166:167], v[170:171]
	v_cvt_pk_bf16_f32 v0, v28, v29
	v_cvt_pk_bf16_f32 v1, v86, v87
	v_cvt_pk_bf16_f32 v3, v88, v89
	v_mov_b32_e32 v76, v152
	v_mov_b32_e32 v250, v172
	v_mov_b32_e32 v251, v173
	v_lshlrev_b32_e32 v176, 16, v44
	v_and_b32_e32 v177, 0xffff0000, v44
	v_pk_add_f32 v[108:109], v[108:109], v[176:177] neg_lo:[0,1] neg_hi:[0,1]
	v_cvt_pk_bf16_f32 v172, v108, v109
	v_lshlrev_b32_e32 v178, 16, v45
	v_and_b32_e32 v179, 0xffff0000, v45
	v_pk_add_f32 v[112:113], v[112:113], v[178:179] neg_lo:[0,1] neg_hi:[0,1]
	v_cvt_pk_bf16_f32 v173, v112, v113
	v_lshlrev_b32_e32 v176, 16, v46
	v_and_b32_e32 v177, 0xffff0000, v46
	v_pk_add_f32 v[106:107], v[106:107], v[176:177] neg_lo:[0,1] neg_hi:[0,1]
	v_cvt_pk_bf16_f32 v174, v106, v107
	v_lshlrev_b32_e32 v178, 16, v47
	v_and_b32_e32 v179, 0xffff0000, v47
	v_pk_add_f32 v[110:111], v[110:111], v[178:179] neg_lo:[0,1] neg_hi:[0,1]
	v_cvt_pk_bf16_f32 v175, v110, v111
	s_waitcnt vmcnt(10)
	v_mfma_f32_16x16x32_bf16 v[160:163], v[44:47], v[186:189], 0
	v_mfma_f32_16x16x32_bf16 v[164:167], v[44:47], v[194:197], 0
	v_mfma_f32_16x16x32_bf16 v[168:171], v[44:47], v[202:205], 0
	v_mfma_f32_16x16x32_bf16 v[160:163], v[44:47], v[190:193], v[160:163]
	v_mfma_f32_16x16x32_bf16 v[164:167], v[44:47], v[198:201], v[164:167]
	v_mfma_f32_16x16x32_bf16 v[168:171], v[44:47], v[206:209], v[168:171]
	v_mfma_f32_16x16x32_bf16 v[160:163], v[172:175], v[186:189], v[160:163]
	v_mfma_f32_16x16x32_bf16 v[164:167], v[172:175], v[194:197], v[164:167]
	v_mfma_f32_16x16x32_bf16 v[168:171], v[172:175], v[202:205], v[168:171]
	s_add_u32 s100, s22, 0x4000
	s_addc_u32 s101, s23, 0
	global_load_dwordx4 v[186:189], v152, s[100:101]
	global_load_dwordx4 v[190:193], v152, s[100:101] offset:1024
	global_load_dwordx4 v[194:197], v152, s[100:101] offset:2048
	global_load_dwordx4 v[198:201], v152, s[100:101] offset:3072
	s_add_u32 s100, s22, 0x5000
	s_addc_u32 s101, s23, 0
	global_load_dwordx4 v[202:205], v152, s[100:101]
	global_load_dwordx4 v[206:209], v152, s[100:101] offset:1024
	v_lshlrev_b32_e32 v176, 16, v24
	v_and_b32_e32 v177, 0xffff0000, v24
	v_pk_add_f32 v[98:99], v[98:99], v[176:177] neg_lo:[0,1] neg_hi:[0,1]
	v_cvt_pk_bf16_f32 v172, v98, v99
	v_lshlrev_b32_e32 v178, 16, v25
	v_and_b32_e32 v179, 0xffff0000, v25
	v_pk_add_f32 v[102:103], v[102:103], v[178:179] neg_lo:[0,1] neg_hi:[0,1]
	v_cvt_pk_bf16_f32 v173, v102, v103
	v_lshlrev_b32_e32 v176, 16, v26
	v_and_b32_e32 v177, 0xffff0000, v26
	v_pk_add_f32 v[100:101], v[100:101], v[176:177] neg_lo:[0,1] neg_hi:[0,1]
	v_cvt_pk_bf16_f32 v174, v100, v101
	v_lshlrev_b32_e32 v178, 16, v27
	v_and_b32_e32 v179, 0xffff0000, v27
	v_pk_add_f32 v[104:105], v[104:105], v[178:179] neg_lo:[0,1] neg_hi:[0,1]
	v_cvt_pk_bf16_f32 v175, v104, v105
	s_waitcnt vmcnt(10)
	v_mfma_f32_16x16x32_bf16 v[160:163], v[24:27], v[210:213], v[160:163]
	v_mfma_f32_16x16x32_bf16 v[164:167], v[24:27], v[218:221], v[164:167]
	v_mfma_f32_16x16x32_bf16 v[168:171], v[24:27], v[226:229], v[168:171]
	v_mfma_f32_16x16x32_bf16 v[160:163], v[24:27], v[214:217], v[160:163]
	v_mfma_f32_16x16x32_bf16 v[164:167], v[24:27], v[222:225], v[164:167]
	v_mfma_f32_16x16x32_bf16 v[168:171], v[24:27], v[230:233], v[168:171]
	v_mfma_f32_16x16x32_bf16 v[160:163], v[172:175], v[210:213], v[160:163]
	v_mfma_f32_16x16x32_bf16 v[164:167], v[172:175], v[218:221], v[164:167]
	v_mfma_f32_16x16x32_bf16 v[168:171], v[172:175], v[226:229], v[168:171]
	global_load_dwordx4 v[210:213], v152, s[100:101] offset:2048
	global_load_dwordx4 v[214:217], v152, s[100:101] offset:3072
	s_add_u32 s100, s22, 0x6000
	s_addc_u32 s101, s23, 0
	global_load_dwordx4 v[218:221], v152, s[100:101]
	global_load_dwordx4 v[222:225], v152, s[100:101] offset:1024
	global_load_dwordx4 v[226:229], v152, s[100:101] offset:2048
	global_load_dwordx4 v[230:233], v152, s[100:101] offset:3072
	v_lshlrev_b32_e32 v176, 16, v4
	v_and_b32_e32 v177, 0xffff0000, v4
	v_pk_add_f32 v[90:91], v[90:91], v[176:177] neg_lo:[0,1] neg_hi:[0,1]
	v_cvt_pk_bf16_f32 v172, v90, v91
	v_lshlrev_b32_e32 v178, 16, v5
	v_and_b32_e32 v179, 0xffff0000, v5
	v_pk_add_f32 v[94:95], v[94:95], v[178:179] neg_lo:[0,1] neg_hi:[0,1]
	v_cvt_pk_bf16_f32 v173, v94, v95
	v_lshlrev_b32_e32 v176, 16, v6
	v_and_b32_e32 v177, 0xffff0000, v6
	v_pk_add_f32 v[92:93], v[92:93], v[176:177] neg_lo:[0,1] neg_hi:[0,1]
	v_cvt_pk_bf16_f32 v174, v92, v93
	v_lshlrev_b32_e32 v178, 16, v7
	v_and_b32_e32 v179, 0xffff0000, v7
	v_pk_add_f32 v[96:97], v[96:97], v[178:179] neg_lo:[0,1] neg_hi:[0,1]
	v_cvt_pk_bf16_f32 v175, v96, v97
	s_waitcnt vmcnt(10)
; #define RT_LOAD(fr, c) do { _Pragma("unroll") for (int i = 0; i < 16; ++i) fr[i] = WFRAG((c) * 16 + i); } while (0)
; template <int MODE>
; __device__ __forceinline__ void norm_phase(const MkArgs& a, LAS unsigned char* lds, const int l, const int wv) {
;     ...
;             u32x4 frA[16], frB[16];
;     ...
;             RT_LOAD(frA, 0); RT_LOAD(frB, 1);
;             RT_MMA(frA, 0);
;             RT_LOAD(frA, 2);
;             RT_MMA(frB, 1);
;             RT_MMA(frA, 2);
	v_mfma_f32_16x16x32_bf16 v[160:163], v[4:7], v[234:237], v[160:163]
	v_mfma_f32_16x16x32_bf16 v[164:167], v[4:7], v[242:245], v[164:167]
	v_mfma_f32_16x16x32_bf16 v[168:171], v[4:7], v[186:189], v[168:171]
	v_mfma_f32_16x16x32_bf16 v[160:163], v[4:7], v[238:241], v[160:163]
	v_mfma_f32_16x16x32_bf16 v[164:167], v[4:7], v[246:249], v[164:167]
	v_mfma_f32_16x16x32_bf16 v[168:171], v[4:7], v[190:193], v[168:171]
	v_mfma_f32_16x16x32_bf16 v[160:163], v[172:175], v[234:237], v[160:163]
	v_mfma_f32_16x16x32_bf16 v[164:167], v[172:175], v[242:245], v[164:167]
	v_mfma_f32_16x16x32_bf16 v[168:171], v[172:175], v[186:189], v[168:171]
	s_add_u32 s100, s22, 0x7000
	s_addc_u32 s101, s23, 0
	global_load_dwordx4 v[234:237], v152, s[100:101]
	global_load_dwordx4 v[238:241], v152, s[100:101] offset:1024
	global_load_dwordx4 v[242:245], v152, s[100:101] offset:2048
	global_load_dwordx4 v[246:249], v152, s[100:101] offset:3072
	s_add_u32 s100, s22, 0x8000
	s_addc_u32 s101, s23, 0
	global_load_dwordx4 v[186:189], v152, s[100:101]
	global_load_dwordx4 v[190:193], v152, s[100:101] offset:1024
	v_lshlrev_b32_e32 v176, 16, v8
	v_and_b32_e32 v177, 0xffff0000, v8
	v_pk_add_f32 v[48:49], v[48:49], v[176:177] neg_lo:[0,1] neg_hi:[0,1]
	v_cvt_pk_bf16_f32 v172, v48, v49
	v_lshlrev_b32_e32 v178, 16, v9
	v_and_b32_e32 v179, 0xffff0000, v9
	v_pk_add_f32 v[52:53], v[52:53], v[178:179] neg_lo:[0,1] neg_hi:[0,1]
	v_cvt_pk_bf16_f32 v173, v52, v53
	v_lshlrev_b32_e32 v176, 16, v10
	v_and_b32_e32 v177, 0xffff0000, v10
	v_pk_add_f32 v[50:51], v[50:51], v[176:177] neg_lo:[0,1] neg_hi:[0,1]
	v_cvt_pk_bf16_f32 v174, v50, v51
	v_lshlrev_b32_e32 v178, 16, v11
	v_and_b32_e32 v179, 0xffff0000, v11
	v_pk_add_f32 v[54:55], v[54:55], v[178:179] neg_lo:[0,1] neg_hi:[0,1]
	v_cvt_pk_bf16_f32 v175, v54, v55
	s_waitcnt vmcnt(10)
	v_mfma_f32_16x16x32_bf16 v[160:163], v[8:11], v[194:197], v[160:163]
	v_mfma_f32_16x16x32_bf16 v[164:167], v[8:11], v[202:205], v[164:167]
	v_mfma_f32_16x16x32_bf16 v[168:171], v[8:11], v[210:213], v[168:171]
	v_mfma_f32_16x16x32_bf16 v[160:163], v[8:11], v[198:201], v[160:163]
	v_mfma_f32_16x16x32_bf16 v[164:167], v[8:11], v[206:209], v[164:167]
	v_mfma_f32_16x16x32_bf16 v[168:171], v[8:11], v[214:217], v[168:171]
	v_mfma_f32_16x16x32_bf16 v[160:163], v[172:175], v[194:197], v[160:163]
	v_mfma_f32_16x16x32_bf16 v[164:167], v[172:175], v[202:205], v[164:167]
	v_mfma_f32_16x16x32_bf16 v[168:171], v[172:175], v[210:213], v[168:171]
	global_load_dwordx4 v[194:197], v152, s[100:101] offset:2048
	global_load_dwordx4 v[198:201], v152, s[100:101] offset:3072
	s_add_u32 s100, s22, 0x9000
	s_addc_u32 s101, s23, 0
	global_load_dwordx4 v[202:205], v152, s[100:101]
	global_load_dwordx4 v[206:209], v152, s[100:101] offset:1024
	global_load_dwordx4 v[210:213], v152, s[100:101] offset:2048
	global_load_dwordx4 v[214:217], v152, s[100:101] offset:3072
	v_lshlrev_b32_e32 v176, 16, v12
	v_and_b32_e32 v177, 0xffff0000, v12
	v_pk_add_f32 v[40:41], v[40:41], v[176:177] neg_lo:[0,1] neg_hi:[0,1]
	v_cvt_pk_bf16_f32 v172, v40, v41
	v_lshlrev_b32_e32 v178, 16, v13
	v_and_b32_e32 v179, 0xffff0000, v13
	v_pk_add_f32 v[56:57], v[56:57], v[178:179] neg_lo:[0,1] neg_hi:[0,1]
	v_cvt_pk_bf16_f32 v173, v56, v57
	v_lshlrev_b32_e32 v176, 16, v14
	v_and_b32_e32 v177, 0xffff0000, v14
	v_pk_add_f32 v[42:43], v[42:43], v[176:177] neg_lo:[0,1] neg_hi:[0,1]
	v_cvt_pk_bf16_f32 v174, v42, v43
	v_lshlrev_b32_e32 v178, 16, v15
	v_and_b32_e32 v179, 0xffff0000, v15
	v_pk_add_f32 v[58:59], v[58:59], v[178:179] neg_lo:[0,1] neg_hi:[0,1]
	v_cvt_pk_bf16_f32 v175, v58, v59
	s_waitcnt vmcnt(10)
	v_mfma_f32_16x16x32_bf16 v[160:163], v[12:15], v[218:221], v[160:163]
	v_mfma_f32_16x16x32_bf16 v[164:167], v[12:15], v[226:229], v[164:167]
	v_mfma_f32_16x16x32_bf16 v[168:171], v[12:15], v[234:237], v[168:171]
	v_mfma_f32_16x16x32_bf16 v[160:163], v[12:15], v[222:225], v[160:163]
	v_mfma_f32_16x16x32_bf16 v[164:167], v[12:15], v[230:233], v[164:167]
	v_mfma_f32_16x16x32_bf16 v[168:171], v[12:15], v[238:241], v[168:171]
	v_mfma_f32_16x16x32_bf16 v[160:163], v[172:175], v[218:221], v[160:163]
	v_mfma_f32_16x16x32_bf16 v[164:167], v[172:175], v[226:229], v[164:167]
	v_mfma_f32_16x16x32_bf16 v[168:171], v[172:175], v[234:237], v[168:171]
	s_add_u32 s100, s22, 0xa000
	s_addc_u32 s101, s23, 0
	global_load_dwordx4 v[218:221], v152, s[100:101]
	global_load_dwordx4 v[222:225], v152, s[100:101] offset:1024
	global_load_dwordx4 v[226:229], v152, s[100:101] offset:2048
	global_load_dwordx4 v[230:233], v152, s[100:101] offset:3072
	s_add_u32 s100, s22, 0xb000
	s_addc_u32 s101, s23, 0
	global_load_dwordx4 v[234:237], v152, s[100:101]
	global_load_dwordx4 v[238:241], v152, s[100:101] offset:1024
	v_lshlrev_b32_e32 v176, 16, v16
	v_and_b32_e32 v177, 0xffff0000, v16
	v_pk_add_f32 v[36:37], v[36:37], v[176:177] neg_lo:[0,1] neg_hi:[0,1]
	v_cvt_pk_bf16_f32 v172, v36, v37
	v_lshlrev_b32_e32 v178, 16, v17
	v_and_b32_e32 v179, 0xffff0000, v17
	v_pk_add_f32 v[60:61], v[60:61], v[178:179] neg_lo:[0,1] neg_hi:[0,1]
	v_cvt_pk_bf16_f32 v173, v60, v61
	v_lshlrev_b32_e32 v176, 16, v18
	v_and_b32_e32 v177, 0xffff0000, v18
	v_pk_add_f32 v[38:39], v[38:39], v[176:177] neg_lo:[0,1] neg_hi:[0,1]
	v_cvt_pk_bf16_f32 v174, v38, v39
	v_lshlrev_b32_e32 v178, 16, v19
	v_and_b32_e32 v179, 0xffff0000, v19
	v_pk_add_f32 v[62:63], v[62:63], v[178:179] neg_lo:[0,1] neg_hi:[0,1]
	v_cvt_pk_bf16_f32 v175, v62, v63
	s_waitcnt vmcnt(10)
; #define RT_LOAD(fr, c) do { _Pragma("unroll") for (int i = 0; i < 16; ++i) fr[i] = WFRAG((c) * 16 + i); } while (0)
; template <int MODE>
; __device__ __forceinline__ void norm_phase(const MkArgs& a, LAS unsigned char* lds, const int l, const int wv) {
;     ...
;                 *(u32x4*)(hb + (size_t)t * DM + k) = o;
;     ...
;             RT_LOAD(frA, 0); RT_LOAD(frB, 1);
;             RT_MMA(frA, 0);
;             RT_LOAD(frA, 2);
;             RT_MMA(frB, 1);
;             RT_MMA(frA, 2);
;     ...
; #pragma unroll
;             for (int nt = 0; nt < 3; ++nt)
; #pragma unroll
;                 for (int e = 0; e < 4; ++e) part[(w * 16 + 4 * q + e) * 48 + 16 * nt + r] = acc[nt][e];
;     ...
;             __syncthreads();
	v_mfma_f32_16x16x32_bf16 v[160:163], v[16:19], v[242:245], v[160:163]
	v_mfma_f32_16x16x32_bf16 v[164:167], v[16:19], v[186:189], v[164:167]
	v_mfma_f32_16x16x32_bf16 v[168:171], v[16:19], v[194:197], v[168:171]
	v_mfma_f32_16x16x32_bf16 v[160:163], v[16:19], v[246:249], v[160:163]
	v_mfma_f32_16x16x32_bf16 v[164:167], v[16:19], v[190:193], v[164:167]
	v_mfma_f32_16x16x32_bf16 v[168:171], v[16:19], v[198:201], v[168:171]
	v_mfma_f32_16x16x32_bf16 v[160:163], v[172:175], v[242:245], v[160:163]
	v_mfma_f32_16x16x32_bf16 v[164:167], v[172:175], v[186:189], v[164:167]
	v_mfma_f32_16x16x32_bf16 v[168:171], v[172:175], v[194:197], v[168:171]
	global_load_dwordx4 v[242:245], v152, s[100:101] offset:2048
	global_load_dwordx4 v[246:249], v152, s[100:101] offset:3072
	v_lshlrev_b32_e32 v176, 16, v20
	v_and_b32_e32 v177, 0xffff0000, v20
	v_pk_add_f32 v[32:33], v[32:33], v[176:177] neg_lo:[0,1] neg_hi:[0,1]
	v_cvt_pk_bf16_f32 v172, v32, v33
	v_lshlrev_b32_e32 v178, 16, v21
	v_and_b32_e32 v179, 0xffff0000, v21
	v_pk_add_f32 v[82:83], v[82:83], v[178:179] neg_lo:[0,1] neg_hi:[0,1]
	v_cvt_pk_bf16_f32 v173, v82, v83
	v_lshlrev_b32_e32 v176, 16, v22
	v_and_b32_e32 v177, 0xffff0000, v22
	v_pk_add_f32 v[34:35], v[34:35], v[176:177] neg_lo:[0,1] neg_hi:[0,1]
	v_cvt_pk_bf16_f32 v174, v34, v35
	v_lshlrev_b32_e32 v178, 16, v23
	v_and_b32_e32 v179, 0xffff0000, v23
	v_pk_add_f32 v[84:85], v[84:85], v[178:179] neg_lo:[0,1] neg_hi:[0,1]
	v_cvt_pk_bf16_f32 v175, v84, v85
	s_waitcnt vmcnt(6)
	v_mfma_f32_16x16x32_bf16 v[160:163], v[20:23], v[202:205], v[160:163]
	v_mfma_f32_16x16x32_bf16 v[164:167], v[20:23], v[210:213], v[164:167]
	v_mfma_f32_16x16x32_bf16 v[168:171], v[20:23], v[218:221], v[168:171]
	v_mfma_f32_16x16x32_bf16 v[160:163], v[20:23], v[206:209], v[160:163]
	v_mfma_f32_16x16x32_bf16 v[164:167], v[20:23], v[214:217], v[164:167]
	v_mfma_f32_16x16x32_bf16 v[168:171], v[20:23], v[222:225], v[168:171]
	v_mfma_f32_16x16x32_bf16 v[160:163], v[172:175], v[202:205], v[160:163]
	v_mfma_f32_16x16x32_bf16 v[164:167], v[172:175], v[210:213], v[164:167]
	v_mfma_f32_16x16x32_bf16 v[168:171], v[172:175], v[218:221], v[168:171]
	v_lshlrev_b32_e32 v176, 16, v0
	v_and_b32_e32 v177, 0xffff0000, v0
	v_pk_add_f32 v[28:29], v[28:29], v[176:177] neg_lo:[0,1] neg_hi:[0,1]
	v_cvt_pk_bf16_f32 v172, v28, v29
	v_lshlrev_b32_e32 v178, 16, v1
	v_and_b32_e32 v179, 0xffff0000, v1
	v_pk_add_f32 v[86:87], v[86:87], v[178:179] neg_lo:[0,1] neg_hi:[0,1]
	v_cvt_pk_bf16_f32 v173, v86, v87
	v_lshlrev_b32_e32 v176, 16, v2
	v_and_b32_e32 v177, 0xffff0000, v2
	v_pk_add_f32 v[30:31], v[30:31], v[176:177] neg_lo:[0,1] neg_hi:[0,1]
	v_cvt_pk_bf16_f32 v174, v30, v31
	v_lshlrev_b32_e32 v178, 16, v3
	v_and_b32_e32 v179, 0xffff0000, v3
	v_pk_add_f32 v[88:89], v[88:89], v[178:179] neg_lo:[0,1] neg_hi:[0,1]
	v_cvt_pk_bf16_f32 v175, v88, v89
	s_waitcnt vmcnt(0)
	v_mfma_f32_16x16x32_bf16 v[160:163], v[0:3], v[226:229], v[160:163]
	v_mfma_f32_16x16x32_bf16 v[164:167], v[0:3], v[234:237], v[164:167]
	v_mfma_f32_16x16x32_bf16 v[168:171], v[0:3], v[242:245], v[168:171]
	v_mfma_f32_16x16x32_bf16 v[160:163], v[0:3], v[230:233], v[160:163]
	v_mfma_f32_16x16x32_bf16 v[164:167], v[0:3], v[238:241], v[164:167]
	v_mfma_f32_16x16x32_bf16 v[168:171], v[0:3], v[246:249], v[168:171]
	v_mfma_f32_16x16x32_bf16 v[160:163], v[172:175], v[226:229], v[160:163]
	v_mfma_f32_16x16x32_bf16 v[164:167], v[172:175], v[234:237], v[164:167]
	v_mfma_f32_16x16x32_bf16 v[168:171], v[172:175], v[242:245], v[168:171]
	global_store_dwordx4 v[250:251], v[44:47], off
	global_store_dwordx4 v[250:251], v[24:27], off offset:64
	global_store_dwordx4 v[250:251], v[4:7], off offset:128
	global_store_dwordx4 v[250:251], v[8:11], off offset:192
	global_store_dwordx4 v[250:251], v[12:15], off offset:256
	global_store_dwordx4 v[250:251], v[16:19], off offset:320
	global_store_dwordx4 v[250:251], v[20:23], off offset:384
	global_store_dwordx4 v[250:251], v[0:3], off offset:448
	v_add_u32_e32 v4, 0x400, v156
	s_nop 7
	s_nop 1
	ds_write2_b32 v4, v160, v164 offset1:16
	ds_write2_b32 v4, v162, v166 offset0:96 offset1:112
	ds_write2_b32 v4, v168, v161 offset0:32 offset1:48
	ds_write2_b32 v4, v165, v169 offset0:64 offset1:80
	ds_write2_b32 v4, v170, v163 offset0:128 offset1:144
	ds_write2_b32 v4, v167, v171 offset0:160 offset1:176
	s_waitcnt lgkmcnt(0)
	s_barrier
	s_and_saveexec_b64 s[12:13], s[4:5]
	s_cbranch_execz .LBB0_904
	s_mov_b64 s[14:15], 0
	v_mov_b32_e32 v0, v114
	v_mov_b32_e32 v2, v64

; template <int MODE>
; __device__ __forceinline__ void norm_phase(const MkArgs& a, LAS unsigned char* lds, const int l, const int wv) {
;     ...
;         float xv[64];
; #pragma unroll
;         for (int j = 0; j < 8; ++j) {
;             const int k = 256 * w + 32 * j + 8 * q;
;             const f32x4 v0 = *(const f32x4*)(xsrc + (size_t)t * DM + k), v1 = *(const f32x4*)(xsrc + (size_t)t * DM + k + 4);
;             xv[8 * j + 0] = v0[0]; xv[8 * j + 1] = v0[1]; xv[8 * j + 2] = v0[2]; xv[8 * j + 3] = v0[3];
;             xv[8 * j + 4] = v1[0]; xv[8 * j + 5] = v1[1]; xv[8 * j + 6] = v1[2]; xv[8 * j + 7] = v1[3];
;         }
;         if constexpr (MODE == 1 || MODE == 3) {
;             const float* tokw = (const float*)(ws + WS_TOKW);
;             const bf16_t* yb = (const bf16_t*)(ws + WS_YB);
;             const float w0 = tokw[2 * t], w1 = tokw[2 * t + 1];
; #pragma unroll
;             for (int j = 0; j < 8; ++j) {
;                 const int k = 256 * w + 32 * j + 8 * q;
;                 const u32x4 y0 = *(const u32x4*)(yb + (size_t)(2 * t) * DM + k), y1 = *(const u32x4*)(yb + (size_t)(2 * t + 1) * DM + k);
;                 const f32x4 g0 = *(const LAS f32x4*)&tabG[k], g1 = *(const LAS f32x4*)&tabG[k + 4];
;                 xv[8 * j + 0] += g0[0] * (w0 * bf_lo(y0[0]) + w1 * bf_lo(y1[0])); xv[8 * j + 1] += g0[1] * (w0 * bf_hi(y0[0]) + w1 * bf_hi(y1[0]));
;                 xv[8 * j + 2] += g0[2] * (w0 * bf_lo(y0[1]) + w1 * bf_lo(y1[1])); xv[8 * j + 3] += g0[3] * (w0 * bf_hi(y0[1]) + w1 * bf_hi(y1[1]));
;                 xv[8 * j + 4] += g1[0] * (w0 * bf_lo(y0[2]) + w1 * bf_lo(y1[2])); xv[8 * j + 5] += g1[1] * (w0 * bf_hi(y0[2]) + w1 * bf_hi(y1[2]));
;                 xv[8 * j + 6] += g1[2] * (w0 * bf_lo(y0[3]) + w1 * bf_lo(y1[3])); xv[8 * j + 7] += g1[3] * (w0 * bf_hi(y0[3]) + w1 * bf_hi(y1[3]));
;                 if constexpr (MODE == 1) {
;                     *(f32x4*)(xcur + (size_t)t * DM + k) = (f32x4){xv[8 * j + 0], xv[8 * j + 1], xv[8 * j + 2], xv[8 * j + 3]};
;                     *(f32x4*)(xcur + (size_t)t * DM + k + 4) = (f32x4){xv[8 * j + 4], xv[8 * j + 5], xv[8 * j + 6], xv[8 * j + 7]};
;                 }
;             }
;         }
;         float ss = 0.f;
; #pragma unroll
;         for (int i = 0; i < 64; ++i) ss += xv[i] * xv[i];
;         ss += __shfl_xor(ss, 16); ss += __shfl_xor(ss, 32);
;         if (q == 0) ssp[w * 16 + r] = ss;
.LBB0_1971:
	s_lshl_b32 s1, s33, 4
	v_or_b32_e32 v82, s1, v115
	v_ashrrev_i32_e32 v83, 31, v82
	v_lshlrev_b64 v[0:1], 13, v[82:83]
	v_lshl_add_u64 v[0:1], v[72:73], 0, v[0:1]
	global_load_dwordx4 v[60:63], v[0:1], off
	global_load_dwordx4 v[44:47], v[0:1], off offset:16
	global_load_dwordx4 v[56:59], v[0:1], off offset:128
	global_load_dwordx4 v[24:27], v[0:1], off offset:144
	global_load_dwordx4 v[52:55], v[0:1], off offset:256
	global_load_dwordx4 v[4:7], v[0:1], off offset:272
	global_load_dwordx4 v[48:51], v[0:1], off offset:384
	global_load_dwordx4 v[8:11], v[0:1], off offset:400
	global_load_dwordx4 v[40:43], v[0:1], off offset:512
	global_load_dwordx4 v[12:15], v[0:1], off offset:528
	global_load_dwordx4 v[36:39], v[0:1], off offset:640
	global_load_dwordx4 v[16:19], v[0:1], off offset:656
	global_load_dwordx4 v[32:35], v[0:1], off offset:768
	global_load_dwordx4 v[20:23], v[0:1], off offset:784
	global_load_dwordx4 v[28:31], v[0:1], off offset:896
	s_nop 0
	global_load_dwordx4 v[0:3], v[0:1], off offset:912
	global_load_dwordx4 v[186:189], v119, s[22:23]
	global_load_dwordx4 v[190:193], v119, s[22:23] offset:1024
	global_load_dwordx4 v[194:197], v119, s[22:23] offset:2048
	global_load_dwordx4 v[198:201], v119, s[22:23] offset:3072
	s_add_u32 s100, s22, 0x1000
	s_addc_u32 s101, s23, 0
	global_load_dwordx4 v[202:205], v119, s[100:101]
	global_load_dwordx4 v[206:209], v119, s[100:101] offset:1024
	global_load_dwordx4 v[210:213], v119, s[100:101] offset:2048
	global_load_dwordx4 v[214:217], v119, s[100:101] offset:3072
	s_add_u32 s100, s22, 0x2000
	s_addc_u32 s101, s23, 0
	global_load_dwordx4 v[218:221], v119, s[100:101]
	global_load_dwordx4 v[222:225], v119, s[100:101] offset:1024
	global_load_dwordx4 v[226:229], v119, s[100:101] offset:2048
	global_load_dwordx4 v[230:233], v119, s[100:101] offset:3072
	s_add_u32 s100, s22, 0x3000
	s_addc_u32 s101, s23, 0
	global_load_dwordx4 v[234:237], v119, s[100:101]
	global_load_dwordx4 v[238:241], v119, s[100:101] offset:1024
	global_load_dwordx4 v[242:245], v119, s[100:101] offset:2048
	global_load_dwordx4 v[246:249], v119, s[100:101] offset:3072
	s_waitcnt vmcnt(31)
	v_mul_f32_e32 v76, v61, v61
	v_fmac_f32_e32 v76, v60, v60
	v_fmac_f32_e32 v76, v62, v62
	v_fmac_f32_e32 v76, v63, v63
	s_waitcnt vmcnt(30)
	v_fmac_f32_e32 v76, v44, v44
	v_fmac_f32_e32 v76, v45, v45
	v_fmac_f32_e32 v76, v46, v46
	v_fmac_f32_e32 v76, v47, v47
	s_waitcnt vmcnt(29)
	v_fmac_f32_e32 v76, v56, v56
	v_fmac_f32_e32 v76, v57, v57
	v_fmac_f32_e32 v76, v58, v58
	v_fmac_f32_e32 v76, v59, v59
	s_waitcnt vmcnt(28)
	v_fmac_f32_e32 v76, v24, v24
	v_fmac_f32_e32 v76, v25, v25
	v_fmac_f32_e32 v76, v26, v26
	v_fmac_f32_e32 v76, v27, v27
	s_waitcnt vmcnt(27)
	v_fmac_f32_e32 v76, v52, v52
	v_fmac_f32_e32 v76, v53, v53
	v_fmac_f32_e32 v76, v54, v54
	v_fmac_f32_e32 v76, v55, v55
	s_waitcnt vmcnt(26)
	v_fmac_f32_e32 v76, v4, v4
	v_fmac_f32_e32 v76, v5, v5
	v_fmac_f32_e32 v76, v6, v6
	v_fmac_f32_e32 v76, v7, v7
	s_waitcnt vmcnt(25)
	v_fmac_f32_e32 v76, v48, v48
	v_fmac_f32_e32 v76, v49, v49
	v_fmac_f32_e32 v76, v50, v50
	v_fmac_f32_e32 v76, v51, v51
	s_waitcnt vmcnt(24)
	v_fmac_f32_e32 v76, v8, v8
	v_fmac_f32_e32 v76, v9, v9
	v_fmac_f32_e32 v76, v10, v10
	v_fmac_f32_e32 v76, v11, v11
	s_waitcnt vmcnt(23)
	v_fmac_f32_e32 v76, v40, v40
	v_fmac_f32_e32 v76, v41, v41
	v_fmac_f32_e32 v76, v42, v42
	v_fmac_f32_e32 v76, v43, v43
	s_waitcnt vmcnt(22)
	v_fmac_f32_e32 v76, v12, v12
	v_fmac_f32_e32 v76, v13, v13
	v_fmac_f32_e32 v76, v14, v14
	v_fmac_f32_e32 v76, v15, v15
	s_waitcnt vmcnt(21)
	v_fmac_f32_e32 v76, v36, v36
	v_fmac_f32_e32 v76, v37, v37
	v_fmac_f32_e32 v76, v38, v38
	v_fmac_f32_e32 v76, v39, v39
	s_waitcnt vmcnt(20)
	v_fmac_f32_e32 v76, v16, v16
	v_fmac_f32_e32 v76, v17, v17
	v_fmac_f32_e32 v76, v18, v18
	v_fmac_f32_e32 v76, v19, v19
	s_waitcnt vmcnt(19)
	v_fmac_f32_e32 v76, v32, v32
	v_fmac_f32_e32 v76, v33, v33
	v_fmac_f32_e32 v76, v34, v34
	v_fmac_f32_e32 v76, v35, v35
	s_waitcnt vmcnt(18)
	v_fmac_f32_e32 v76, v20, v20
	v_fmac_f32_e32 v76, v21, v21
	v_fmac_f32_e32 v76, v22, v22
	v_fmac_f32_e32 v76, v23, v23
	s_waitcnt vmcnt(17)
	v_fmac_f32_e32 v76, v28, v28
	v_fmac_f32_e32 v76, v29, v29
	v_fmac_f32_e32 v76, v30, v30
	v_fmac_f32_e32 v76, v31, v31
	s_waitcnt vmcnt(16)
	v_fmac_f32_e32 v76, v0, v0
	v_fmac_f32_e32 v76, v1, v1
	v_fmac_f32_e32 v76, v2, v2
	v_fmac_f32_e32 v76, v3, v3
	ds_bpermute_b32 v84, v116, v76
	s_waitcnt lgkmcnt(0)
	v_add_f32_e32 v76, v76, v84
	ds_bpermute_b32 v84, v117, v76
	s_and_saveexec_b64 s[12:13], s[4:5]
	s_cbranch_execz .LBB0_1973
	s_waitcnt lgkmcnt(0)
	v_add_f32_e32 v76, v76, v84
	v_add_u32_e32 v84, s26, v118
	ds_write_b32 v84, v76
; #define LAS __attribute__((address_space(3)))
; __device__ __forceinline__ unsigned cvt_pk_bf16(float lo, float hi) { const bf16x2_t r = __builtin_convertvector((f32x2_t){lo, hi}, bf16x2_t); return __builtin_bit_cast(unsigned, r); }
; template <int MODE>
; __device__ __forceinline__ void norm_phase(const MkArgs& a, LAS unsigned char* lds, const int l, const int wv) {
;     ...
;         __syncthreads();
;         float tot = 0.f;
; #pragma unroll
;         for (int i = 0; i < 8; ++i) tot += ssp[i * 16 + r];
;         const float rstd = 1.0f / sqrtf(tot * (1.0f / DM) + EPSV);
; #pragma unroll
;         for (int j = 0; j < 8; ++j) {
;             const int k = 256 * w + 32 * j + 8 * q;
;             const f32x4 g0 = *(const LAS f32x4*)&tabA[k], g1 = *(const LAS f32x4*)&tabA[k + 4];
;             float gg[8] = {g0[0], g0[1], g0[2], g0[3], g1[0], g1[1], g1[2], g1[3]};
;             if constexpr (MODE != 3) {
;                 const f32x4 s0 = *(const LAS f32x4*)&tabB[k], s1 = *(const LAS f32x4*)&tabB[k + 4];
;                 const float sv[8] = {s0[0], s0[1], s0[2], s0[3], s1[0], s1[1], s1[2], s1[3]};
; #pragma unroll
;                 for (int i = 0; i < 8; ++i) xv[8 * j + i] = (xv[8 * j + i] * rstd) * gg[i] + sv[i];
;                 u32x4 o; o[0] = cvt_pk_bf16(xv[8 * j + 0], xv[8 * j + 1]); o[1] = cvt_pk_bf16(xv[8 * j + 2], xv[8 * j + 3]);
;                 o[2] = cvt_pk_bf16(xv[8 * j + 4], xv[8 * j + 5]); o[3] = cvt_pk_bf16(xv[8 * j + 6], xv[8 * j + 7]);
;                 *(u32x4*)(hb + (size_t)t * DM + k) = o;
.LBB0_1973:
	s_or_b64 exec, exec, s[12:13]
	s_waitcnt lgkmcnt(0)
	s_barrier
	ds_read2_b32 v[84:85], v118 offset1:16
	ds_read2_b32 v[86:87], v118 offset0:32 offset1:48
	ds_read2_b32 v[88:89], v118 offset0:64 offset1:80
	s_mov_b32 s12, 0xf800000
	v_lshlrev_b64 v[82:83], 12, v[82:83]
	s_waitcnt lgkmcnt(2)
	v_add_f32_e32 v76, 0, v84
	v_add_f32_e32 v76, v76, v85
	ds_read2_b32 v[84:85], v118 offset0:96 offset1:112
	s_waitcnt lgkmcnt(2)
	v_add_f32_e32 v76, v76, v86
	v_add_f32_e32 v76, v76, v87
	s_waitcnt lgkmcnt(1)
	v_add_f32_e32 v76, v76, v88
	v_add_f32_e32 v76, v76, v89
	s_waitcnt lgkmcnt(0)
	v_add_f32_e32 v76, v76, v84
	v_add_f32_e32 v76, v76, v85
	v_fmamk_f32 v76, v76, 0x3a000000, v154
	v_mul_f32_e32 v84, 0x4f800000, v76
	v_cmp_gt_f32_e32 vcc, s12, v76
	v_lshl_add_u64 v[172:173], v[74:75], 0, v[82:83]
	s_nop 0
	v_cndmask_b32_e32 v76, v76, v84, vcc
	v_sqrt_f32_e32 v84, v76
	s_nop 0
	v_add_u32_e32 v85, -1, v84
	v_fma_f32 v86, -v85, v84, v76
	v_cmp_ge_f32_e64 s[12:13], 0, v86
	v_add_u32_e32 v86, 1, v84
	s_nop 0
	v_cndmask_b32_e64 v85, v84, v85, s[12:13]
	v_fma_f32 v84, -v86, v84, v76
	v_cmp_lt_f32_e64 s[12:13], 0, v84
	s_nop 1
	v_cndmask_b32_e64 v84, v85, v86, s[12:13]
	v_mul_f32_e32 v85, 0x37800000, v84
	v_cndmask_b32_e32 v84, v84, v85, vcc
	v_cmp_class_f32_e32 vcc, v76, v155
	s_nop 1
	v_cndmask_b32_e32 v76, v84, v76, vcc
	v_div_scale_f32 v84, s[12:13], v76, v76, 1.0
	v_rcp_f32_e32 v85, v84
	s_movk_i32 s12, 0x2000
	v_fma_f32 v86, -v84, v85, 1.0
	v_fmac_f32_e32 v85, v86, v85
	v_div_scale_f32 v86, vcc, 1.0, v76, 1.0
	v_mul_f32_e32 v87, v86, v85
	v_fma_f32 v88, -v84, v87, v86
	v_fmac_f32_e32 v87, v88, v85
	v_fma_f32 v84, -v84, v87, v86
	v_div_fmas_f32 v84, v84, v85, v87
	v_div_fixup_f32 v76, v84, v76, 1.0
	ds_read_b128 v[84:87], v65
	ds_read_b128 v[88:91], v124
	ds_read_b128 v[92:95], v123
	ds_read_b128 v[96:99], v125
	v_pk_mul_f32 v[60:61], v[60:61], v[76:77] op_sel_hi:[1,0]
	v_pk_mul_f32 v[44:45], v[44:45], v[76:77] op_sel_hi:[1,0]
	v_pk_mul_f32 v[56:57], v[56:57], v[76:77] op_sel_hi:[1,0]
	s_waitcnt lgkmcnt(2)
	v_pk_fma_f32 v[108:109], v[84:85], v[60:61], v[88:89]
	v_pk_mul_f32 v[60:61], v[62:63], v[76:77] op_sel_hi:[1,0]
	s_waitcnt lgkmcnt(0)
	v_pk_fma_f32 v[106:107], v[92:93], v[44:45], v[96:97]
	v_pk_mul_f32 v[44:45], v[46:47], v[76:77] op_sel_hi:[1,0]
	v_pk_fma_f32 v[112:113], v[86:87], v[60:61], v[90:91]
	v_pk_fma_f32 v[110:111], v[94:95], v[44:45], v[98:99]
	v_cvt_pk_bf16_f32 v44, v108, v109
	v_cvt_pk_bf16_f32 v45, v112, v113
	v_cvt_pk_bf16_f32 v46, v106, v107
	v_cvt_pk_bf16_f32 v47, v110, v111
	ds_read_b128 v[60:63], v126
	ds_read_b128 v[82:85], v128
	ds_read_b128 v[86:89], v127
	ds_read_b128 v[90:93], v129
	v_pk_mul_f32 v[24:25], v[24:25], v[76:77] op_sel_hi:[1,0]
	v_pk_mul_f32 v[52:53], v[52:53], v[76:77] op_sel_hi:[1,0]
	s_waitcnt lgkmcnt(2)
	v_pk_fma_f32 v[98:99], v[56:57], v[60:61], v[82:83]
	v_pk_mul_f32 v[56:57], v[58:59], v[76:77] op_sel_hi:[1,0]
	s_waitcnt lgkmcnt(0)
	v_pk_fma_f32 v[100:101], v[24:25], v[86:87], v[90:91]
	v_pk_mul_f32 v[24:25], v[26:27], v[76:77] op_sel_hi:[1,0]
	v_pk_fma_f32 v[102:103], v[56:57], v[62:63], v[84:85]
	v_pk_fma_f32 v[104:105], v[24:25], v[88:89], v[92:93]
	v_cvt_pk_bf16_f32 v24, v98, v99
	v_cvt_pk_bf16_f32 v25, v102, v103
	v_cvt_pk_bf16_f32 v26, v100, v101
	v_cvt_pk_bf16_f32 v27, v104, v105
	ds_read_b128 v[56:59], v130
	ds_read_b128 v[60:63], v132
	ds_read_b128 v[82:85], v131
	ds_read_b128 v[86:89], v133
	v_pk_mul_f32 v[4:5], v[4:5], v[76:77] op_sel_hi:[1,0]
	v_pk_mul_f32 v[48:49], v[48:49], v[76:77] op_sel_hi:[1,0]
	s_waitcnt lgkmcnt(2)
	v_pk_fma_f32 v[90:91], v[52:53], v[56:57], v[60:61]
	v_pk_mul_f32 v[52:53], v[54:55], v[76:77] op_sel_hi:[1,0]
	s_waitcnt lgkmcnt(0)
	v_pk_fma_f32 v[92:93], v[4:5], v[82:83], v[86:87]
	v_pk_mul_f32 v[4:5], v[6:7], v[76:77] op_sel_hi:[1,0]
	v_pk_fma_f32 v[94:95], v[52:53], v[58:59], v[62:63]
	v_pk_fma_f32 v[96:97], v[4:5], v[84:85], v[88:89]
	v_cvt_pk_bf16_f32 v4, v90, v91
	v_cvt_pk_bf16_f32 v5, v94, v95
	v_cvt_pk_bf16_f32 v6, v92, v93
	v_cvt_pk_bf16_f32 v7, v96, v97
	ds_read_b128 v[52:55], v134
	ds_read_b128 v[56:59], v136
	ds_read_b128 v[60:63], v135
	ds_read_b128 v[82:85], v137
	v_pk_mul_f32 v[50:51], v[50:51], v[76:77] op_sel_hi:[1,0]
	v_pk_mul_f32 v[8:9], v[8:9], v[76:77] op_sel_hi:[1,0]
	s_waitcnt lgkmcnt(2)
	v_pk_fma_f32 v[48:49], v[48:49], v[52:53], v[56:57]
	v_pk_fma_f32 v[52:53], v[50:51], v[54:55], v[58:59]
	s_waitcnt lgkmcnt(0)
	v_pk_fma_f32 v[50:51], v[8:9], v[60:61], v[82:83]
	v_pk_mul_f32 v[8:9], v[10:11], v[76:77] op_sel_hi:[1,0]
	v_cvt_pk_bf16_f32 v10, v50, v51
	v_pk_fma_f32 v[54:55], v[8:9], v[62:63], v[84:85]
	v_cvt_pk_bf16_f32 v8, v48, v49
	v_cvt_pk_bf16_f32 v9, v52, v53
	v_cvt_pk_bf16_f32 v11, v54, v55
	ds_read_b128 v[56:59], v138
	ds_read_b128 v[60:63], v140
	ds_read_b128 v[82:85], v139
	ds_read_b128 v[86:89], v141
	v_pk_mul_f32 v[40:41], v[40:41], v[76:77] op_sel_hi:[1,0]
	v_pk_mul_f32 v[42:43], v[42:43], v[76:77] op_sel_hi:[1,0]
	v_pk_mul_f32 v[12:13], v[12:13], v[76:77] op_sel_hi:[1,0]
	s_waitcnt lgkmcnt(2)
	v_pk_fma_f32 v[40:41], v[40:41], v[56:57], v[60:61]
	v_pk_fma_f32 v[56:57], v[42:43], v[58:59], v[62:63]
	s_waitcnt lgkmcnt(0)
	v_pk_fma_f32 v[42:43], v[12:13], v[82:83], v[86:87]
	v_pk_mul_f32 v[12:13], v[14:15], v[76:77] op_sel_hi:[1,0]
	v_cvt_pk_bf16_f32 v14, v42, v43
	v_pk_fma_f32 v[58:59], v[12:13], v[84:85], v[88:89]
	v_cvt_pk_bf16_f32 v12, v40, v41
	v_cvt_pk_bf16_f32 v13, v56, v57
	v_cvt_pk_bf16_f32 v15, v58, v59
	ds_read_b128 v[60:63], v142
	ds_read_b128 v[82:85], v144
	ds_read_b128 v[86:89], v143
	ds_read_b128 v[160:163], v145
	v_pk_mul_f32 v[36:37], v[36:37], v[76:77] op_sel_hi:[1,0]
	v_pk_mul_f32 v[38:39], v[38:39], v[76:77] op_sel_hi:[1,0]
	v_pk_mul_f32 v[16:17], v[16:17], v[76:77] op_sel_hi:[1,0]
	s_waitcnt lgkmcnt(2)
; #define LAS __attribute__((address_space(3)))
; __device__ __forceinline__ unsigned cvt_pk_bf16(float lo, float hi) { const bf16x2_t r = __builtin_convertvector((f32x2_t){lo, hi}, bf16x2_t); return __builtin_bit_cast(unsigned, r); }
; #define RT_LOAD(fr, c) do { _Pragma("unroll") for (int i = 0; i < 16; ++i) fr[i] = WFRAG((c) * 16 + i); } while (0)
; template <int MODE>
; __device__ __forceinline__ void norm_phase(const MkArgs& a, LAS unsigned char* lds, const int l, const int wv) {
;     ...
;         for (int j = 0; j < 8; ++j) {
;             const int k = 256 * w + 32 * j + 8 * q;
;             const f32x4 g0 = *(const LAS f32x4*)&tabA[k], g1 = *(const LAS f32x4*)&tabA[k + 4];
;             float gg[8] = {g0[0], g0[1], g0[2], g0[3], g1[0], g1[1], g1[2], g1[3]};
;             if constexpr (MODE != 3) {
;                 const f32x4 s0 = *(const LAS f32x4*)&tabB[k], s1 = *(const LAS f32x4*)&tabB[k + 4];
;                 const float sv[8] = {s0[0], s0[1], s0[2], s0[3], s1[0], s1[1], s1[2], s1[3]};
; #pragma unroll
;                 for (int i = 0; i < 8; ++i) xv[8 * j + i] = (xv[8 * j + i] * rstd) * gg[i] + sv[i];
;                 u32x4 o; o[0] = cvt_pk_bf16(xv[8 * j + 0], xv[8 * j + 1]); o[1] = cvt_pk_bf16(xv[8 * j + 2], xv[8 * j + 3]);
;                 o[2] = cvt_pk_bf16(xv[8 * j + 4], xv[8 * j + 5]); o[3] = cvt_pk_bf16(xv[8 * j + 6], xv[8 * j + 7]);
;                 *(u32x4*)(hb + (size_t)t * DM + k) = o;
;     ...
;             RT_LOAD(frA, 0); RT_LOAD(frB, 1);
;             RT_MMA(frA, 0);
;             RT_LOAD(frA, 2);
;             RT_MMA(frB, 1);
	v_pk_fma_f32 v[36:37], v[36:37], v[60:61], v[82:83]
	v_pk_fma_f32 v[60:61], v[38:39], v[62:63], v[84:85]
	s_waitcnt lgkmcnt(0)
	v_pk_fma_f32 v[38:39], v[16:17], v[86:87], v[160:161]
	v_pk_mul_f32 v[16:17], v[18:19], v[76:77] op_sel_hi:[1,0]
	v_cvt_pk_bf16_f32 v18, v38, v39
	v_pk_fma_f32 v[62:63], v[16:17], v[88:89], v[162:163]
	v_cvt_pk_bf16_f32 v16, v36, v37
	v_cvt_pk_bf16_f32 v17, v60, v61
	v_cvt_pk_bf16_f32 v19, v62, v63
	ds_read_b128 v[82:85], v146
	ds_read_b128 v[86:89], v148
	ds_read_b128 v[160:163], v147
	ds_read_b128 v[164:167], v149
	v_pk_mul_f32 v[32:33], v[32:33], v[76:77] op_sel_hi:[1,0]
	v_pk_mul_f32 v[34:35], v[34:35], v[76:77] op_sel_hi:[1,0]
	v_pk_mul_f32 v[20:21], v[20:21], v[76:77] op_sel_hi:[1,0]
	s_waitcnt lgkmcnt(2)
	v_pk_fma_f32 v[32:33], v[32:33], v[82:83], v[86:87]
	v_pk_fma_f32 v[82:83], v[34:35], v[84:85], v[88:89]
	s_waitcnt lgkmcnt(0)
	v_pk_fma_f32 v[34:35], v[20:21], v[160:161], v[164:165]
	v_pk_mul_f32 v[20:21], v[22:23], v[76:77] op_sel_hi:[1,0]
	v_cvt_pk_bf16_f32 v22, v34, v35
	v_pk_fma_f32 v[84:85], v[20:21], v[162:163], v[166:167]
	v_cvt_pk_bf16_f32 v20, v32, v33
	v_cvt_pk_bf16_f32 v21, v82, v83
	v_cvt_pk_bf16_f32 v23, v84, v85
	ds_read_b128 v[86:89], v150
	ds_read_b128 v[160:163], v152
	ds_read_b128 v[164:167], v151
	ds_read_b128 v[168:171], v153
	v_pk_mul_f32 v[28:29], v[28:29], v[76:77] op_sel_hi:[1,0]
	v_pk_mul_f32 v[30:31], v[30:31], v[76:77] op_sel_hi:[1,0]
	v_pk_mul_f32 v[0:1], v[0:1], v[76:77] op_sel_hi:[1,0]
	s_waitcnt lgkmcnt(2)
	v_pk_fma_f32 v[28:29], v[28:29], v[86:87], v[160:161]
	v_pk_fma_f32 v[86:87], v[30:31], v[88:89], v[162:163]
	s_waitcnt lgkmcnt(0)
	v_pk_fma_f32 v[30:31], v[0:1], v[164:165], v[168:169]
	v_pk_mul_f32 v[0:1], v[2:3], v[76:77] op_sel_hi:[1,0]
	v_cvt_pk_bf16_f32 v2, v30, v31
	v_pk_fma_f32 v[88:89], v[0:1], v[166:167], v[170:171]
	v_cvt_pk_bf16_f32 v0, v28, v29
	v_cvt_pk_bf16_f32 v1, v86, v87
	v_cvt_pk_bf16_f32 v3, v88, v89
	v_mov_b32_e32 v76, v119
	v_mov_b32_e32 v250, v172
	v_mov_b32_e32 v251, v173
	v_lshlrev_b32_e32 v176, 16, v44
	v_and_b32_e32 v177, 0xffff0000, v44
	v_pk_add_f32 v[108:109], v[108:109], v[176:177] neg_lo:[0,1] neg_hi:[0,1]
	v_cvt_pk_bf16_f32 v172, v108, v109
	v_lshlrev_b32_e32 v178, 16, v45
	v_and_b32_e32 v179, 0xffff0000, v45
	v_pk_add_f32 v[112:113], v[112:113], v[178:179] neg_lo:[0,1] neg_hi:[0,1]
	v_cvt_pk_bf16_f32 v173, v112, v113
	v_lshlrev_b32_e32 v176, 16, v46
	v_and_b32_e32 v177, 0xffff0000, v46
	v_pk_add_f32 v[106:107], v[106:107], v[176:177] neg_lo:[0,1] neg_hi:[0,1]
	v_cvt_pk_bf16_f32 v174, v106, v107
	v_lshlrev_b32_e32 v178, 16, v47
	v_and_b32_e32 v179, 0xffff0000, v47
	v_pk_add_f32 v[110:111], v[110:111], v[178:179] neg_lo:[0,1] neg_hi:[0,1]
	v_cvt_pk_bf16_f32 v175, v110, v111
	s_waitcnt vmcnt(10)
	v_mfma_f32_16x16x32_bf16 v[160:163], v[44:47], v[186:189], 0
	v_mfma_f32_16x16x32_bf16 v[164:167], v[44:47], v[194:197], 0
	v_mfma_f32_16x16x32_bf16 v[168:171], v[44:47], v[202:205], 0
	v_mfma_f32_16x16x32_bf16 v[160:163], v[44:47], v[190:193], v[160:163]
	v_mfma_f32_16x16x32_bf16 v[164:167], v[44:47], v[198:201], v[164:167]
	v_mfma_f32_16x16x32_bf16 v[168:171], v[44:47], v[206:209], v[168:171]
	v_mfma_f32_16x16x32_bf16 v[160:163], v[172:175], v[186:189], v[160:163]
	v_mfma_f32_16x16x32_bf16 v[164:167], v[172:175], v[194:197], v[164:167]
	v_mfma_f32_16x16x32_bf16 v[168:171], v[172:175], v[202:205], v[168:171]
	s_add_u32 s100, s22, 0x4000
	s_addc_u32 s101, s23, 0
	global_load_dwordx4 v[186:189], v119, s[100:101]
	global_load_dwordx4 v[190:193], v119, s[100:101] offset:1024
	global_load_dwordx4 v[194:197], v119, s[100:101] offset:2048
	global_load_dwordx4 v[198:201], v119, s[100:101] offset:3072
	s_add_u32 s100, s22, 0x5000
	s_addc_u32 s101, s23, 0
	global_load_dwordx4 v[202:205], v119, s[100:101]
	global_load_dwordx4 v[206:209], v119, s[100:101] offset:1024
	v_lshlrev_b32_e32 v176, 16, v24
	v_and_b32_e32 v177, 0xffff0000, v24
	v_pk_add_f32 v[98:99], v[98:99], v[176:177] neg_lo:[0,1] neg_hi:[0,1]
	v_cvt_pk_bf16_f32 v172, v98, v99
	v_lshlrev_b32_e32 v178, 16, v25
	v_and_b32_e32 v179, 0xffff0000, v25
	v_pk_add_f32 v[102:103], v[102:103], v[178:179] neg_lo:[0,1] neg_hi:[0,1]
	v_cvt_pk_bf16_f32 v173, v102, v103
	v_lshlrev_b32_e32 v176, 16, v26
	v_and_b32_e32 v177, 0xffff0000, v26
	v_pk_add_f32 v[100:101], v[100:101], v[176:177] neg_lo:[0,1] neg_hi:[0,1]
	v_cvt_pk_bf16_f32 v174, v100, v101
	v_lshlrev_b32_e32 v178, 16, v27
	v_and_b32_e32 v179, 0xffff0000, v27
	v_pk_add_f32 v[104:105], v[104:105], v[178:179] neg_lo:[0,1] neg_hi:[0,1]
	v_cvt_pk_bf16_f32 v175, v104, v105
	s_waitcnt vmcnt(10)
	v_mfma_f32_16x16x32_bf16 v[160:163], v[24:27], v[210:213], v[160:163]
	v_mfma_f32_16x16x32_bf16 v[164:167], v[24:27], v[218:221], v[164:167]
	v_mfma_f32_16x16x32_bf16 v[168:171], v[24:27], v[226:229], v[168:171]
	v_mfma_f32_16x16x32_bf16 v[160:163], v[24:27], v[214:217], v[160:163]
	v_mfma_f32_16x16x32_bf16 v[164:167], v[24:27], v[222:225], v[164:167]
	v_mfma_f32_16x16x32_bf16 v[168:171], v[24:27], v[230:233], v[168:171]
	v_mfma_f32_16x16x32_bf16 v[160:163], v[172:175], v[210:213], v[160:163]
	v_mfma_f32_16x16x32_bf16 v[164:167], v[172:175], v[218:221], v[164:167]
	v_mfma_f32_16x16x32_bf16 v[168:171], v[172:175], v[226:229], v[168:171]
	global_load_dwordx4 v[210:213], v119, s[100:101] offset:2048
	global_load_dwordx4 v[214:217], v119, s[100:101] offset:3072
	s_add_u32 s100, s22, 0x6000
	s_addc_u32 s101, s23, 0
	global_load_dwordx4 v[218:221], v119, s[100:101]
	global_load_dwordx4 v[222:225], v119, s[100:101] offset:1024
	global_load_dwordx4 v[226:229], v119, s[100:101] offset:2048
	global_load_dwordx4 v[230:233], v119, s[100:101] offset:3072
	v_lshlrev_b32_e32 v176, 16, v4
	v_and_b32_e32 v177, 0xffff0000, v4
	v_pk_add_f32 v[90:91], v[90:91], v[176:177] neg_lo:[0,1] neg_hi:[0,1]
	v_cvt_pk_bf16_f32 v172, v90, v91
	v_lshlrev_b32_e32 v178, 16, v5
	v_and_b32_e32 v179, 0xffff0000, v5
	v_pk_add_f32 v[94:95], v[94:95], v[178:179] neg_lo:[0,1] neg_hi:[0,1]
	v_cvt_pk_bf16_f32 v173, v94, v95
	v_lshlrev_b32_e32 v176, 16, v6
	v_and_b32_e32 v177, 0xffff0000, v6
	v_pk_add_f32 v[92:93], v[92:93], v[176:177] neg_lo:[0,1] neg_hi:[0,1]
	v_cvt_pk_bf16_f32 v174, v92, v93
	v_lshlrev_b32_e32 v178, 16, v7
	v_and_b32_e32 v179, 0xffff0000, v7
	v_pk_add_f32 v[96:97], v[96:97], v[178:179] neg_lo:[0,1] neg_hi:[0,1]
	v_cvt_pk_bf16_f32 v175, v96, v97
	s_waitcnt vmcnt(10)
; #define RT_LOAD(fr, c) do { _Pragma("unroll") for (int i = 0; i < 16; ++i) fr[i] = WFRAG((c) * 16 + i); } while (0)
; template <int MODE>
; __device__ __forceinline__ void norm_phase(const MkArgs& a, LAS unsigned char* lds, const int l, const int wv) {
;     ...
;             RT_LOAD(frA, 0); RT_LOAD(frB, 1);
;             RT_MMA(frA, 0);
;             RT_LOAD(frA, 2);
;             RT_MMA(frB, 1);
	v_mfma_f32_16x16x32_bf16 v[160:163], v[4:7], v[234:237], v[160:163]
	v_mfma_f32_16x16x32_bf16 v[164:167], v[4:7], v[242:245], v[164:167]
	v_mfma_f32_16x16x32_bf16 v[168:171], v[4:7], v[186:189], v[168:171]
	v_mfma_f32_16x16x32_bf16 v[160:163], v[4:7], v[238:241], v[160:163]
	v_mfma_f32_16x16x32_bf16 v[164:167], v[4:7], v[246:249], v[164:167]
	v_mfma_f32_16x16x32_bf16 v[168:171], v[4:7], v[190:193], v[168:171]
	v_mfma_f32_16x16x32_bf16 v[160:163], v[172:175], v[234:237], v[160:163]
	v_mfma_f32_16x16x32_bf16 v[164:167], v[172:175], v[242:245], v[164:167]
	v_mfma_f32_16x16x32_bf16 v[168:171], v[172:175], v[186:189], v[168:171]
	s_add_u32 s100, s22, 0x7000
	s_addc_u32 s101, s23, 0
	global_load_dwordx4 v[234:237], v119, s[100:101]
	global_load_dwordx4 v[238:241], v119, s[100:101] offset:1024
	global_load_dwordx4 v[242:245], v119, s[100:101] offset:2048
	global_load_dwordx4 v[246:249], v119, s[100:101] offset:3072
	s_add_u32 s100, s22, 0x8000
	s_addc_u32 s101, s23, 0
	global_load_dwordx4 v[186:189], v119, s[100:101]
	global_load_dwordx4 v[190:193], v119, s[100:101] offset:1024
	v_lshlrev_b32_e32 v176, 16, v8
	v_and_b32_e32 v177, 0xffff0000, v8
	v_pk_add_f32 v[48:49], v[48:49], v[176:177] neg_lo:[0,1] neg_hi:[0,1]
	v_cvt_pk_bf16_f32 v172, v48, v49
	v_lshlrev_b32_e32 v178, 16, v9
	v_and_b32_e32 v179, 0xffff0000, v9
	v_pk_add_f32 v[52:53], v[52:53], v[178:179] neg_lo:[0,1] neg_hi:[0,1]
	v_cvt_pk_bf16_f32 v173, v52, v53
	v_lshlrev_b32_e32 v176, 16, v10
	v_and_b32_e32 v177, 0xffff0000, v10
	v_pk_add_f32 v[50:51], v[50:51], v[176:177] neg_lo:[0,1] neg_hi:[0,1]
	v_cvt_pk_bf16_f32 v174, v50, v51
	v_lshlrev_b32_e32 v178, 16, v11
	v_and_b32_e32 v179, 0xffff0000, v11
	v_pk_add_f32 v[54:55], v[54:55], v[178:179] neg_lo:[0,1] neg_hi:[0,1]
	v_cvt_pk_bf16_f32 v175, v54, v55
	s_waitcnt vmcnt(10)
	v_mfma_f32_16x16x32_bf16 v[160:163], v[8:11], v[194:197], v[160:163]
	v_mfma_f32_16x16x32_bf16 v[164:167], v[8:11], v[202:205], v[164:167]
	v_mfma_f32_16x16x32_bf16 v[168:171], v[8:11], v[210:213], v[168:171]
	v_mfma_f32_16x16x32_bf16 v[160:163], v[8:11], v[198:201], v[160:163]
	v_mfma_f32_16x16x32_bf16 v[164:167], v[8:11], v[206:209], v[164:167]
	v_mfma_f32_16x16x32_bf16 v[168:171], v[8:11], v[214:217], v[168:171]
	v_mfma_f32_16x16x32_bf16 v[160:163], v[172:175], v[194:197], v[160:163]
	v_mfma_f32_16x16x32_bf16 v[164:167], v[172:175], v[202:205], v[164:167]
	v_mfma_f32_16x16x32_bf16 v[168:171], v[172:175], v[210:213], v[168:171]
	global_load_dwordx4 v[194:197], v119, s[100:101] offset:2048
	global_load_dwordx4 v[198:201], v119, s[100:101] offset:3072
	s_add_u32 s100, s22, 0x9000
	s_addc_u32 s101, s23, 0
	global_load_dwordx4 v[202:205], v119, s[100:101]
	global_load_dwordx4 v[206:209], v119, s[100:101] offset:1024
	global_load_dwordx4 v[210:213], v119, s[100:101] offset:2048
	global_load_dwordx4 v[214:217], v119, s[100:101] offset:3072
	v_lshlrev_b32_e32 v176, 16, v12
	v_and_b32_e32 v177, 0xffff0000, v12
	v_pk_add_f32 v[40:41], v[40:41], v[176:177] neg_lo:[0,1] neg_hi:[0,1]
	v_cvt_pk_bf16_f32 v172, v40, v41
	v_lshlrev_b32_e32 v178, 16, v13
	v_and_b32_e32 v179, 0xffff0000, v13
	v_pk_add_f32 v[56:57], v[56:57], v[178:179] neg_lo:[0,1] neg_hi:[0,1]
	v_cvt_pk_bf16_f32 v173, v56, v57
	v_lshlrev_b32_e32 v176, 16, v14
	v_and_b32_e32 v177, 0xffff0000, v14
	v_pk_add_f32 v[42:43], v[42:43], v[176:177] neg_lo:[0,1] neg_hi:[0,1]
	v_cvt_pk_bf16_f32 v174, v42, v43
	v_lshlrev_b32_e32 v178, 16, v15
	v_and_b32_e32 v179, 0xffff0000, v15
	v_pk_add_f32 v[58:59], v[58:59], v[178:179] neg_lo:[0,1] neg_hi:[0,1]
	v_cvt_pk_bf16_f32 v175, v58, v59
	s_waitcnt vmcnt(10)
	v_mfma_f32_16x16x32_bf16 v[160:163], v[12:15], v[218:221], v[160:163]
	v_mfma_f32_16x16x32_bf16 v[164:167], v[12:15], v[226:229], v[164:167]
	v_mfma_f32_16x16x32_bf16 v[168:171], v[12:15], v[234:237], v[168:171]
	v_mfma_f32_16x16x32_bf16 v[160:163], v[12:15], v[222:225], v[160:163]
	v_mfma_f32_16x16x32_bf16 v[164:167], v[12:15], v[230:233], v[164:167]
	v_mfma_f32_16x16x32_bf16 v[168:171], v[12:15], v[238:241], v[168:171]
	v_mfma_f32_16x16x32_bf16 v[160:163], v[172:175], v[218:221], v[160:163]
	v_mfma_f32_16x16x32_bf16 v[164:167], v[172:175], v[226:229], v[164:167]
	v_mfma_f32_16x16x32_bf16 v[168:171], v[172:175], v[234:237], v[168:171]
	s_add_u32 s100, s22, 0xa000
	s_addc_u32 s101, s23, 0
	global_load_dwordx4 v[218:221], v119, s[100:101]
	global_load_dwordx4 v[222:225], v119, s[100:101] offset:1024
	global_load_dwordx4 v[226:229], v119, s[100:101] offset:2048
	global_load_dwordx4 v[230:233], v119, s[100:101] offset:3072
	s_add_u32 s100, s22, 0xb000
	s_addc_u32 s101, s23, 0
	global_load_dwordx4 v[234:237], v119, s[100:101]
	global_load_dwordx4 v[238:241], v119, s[100:101] offset:1024
	v_lshlrev_b32_e32 v176, 16, v16
	v_and_b32_e32 v177, 0xffff0000, v16
	v_pk_add_f32 v[36:37], v[36:37], v[176:177] neg_lo:[0,1] neg_hi:[0,1]
	v_cvt_pk_bf16_f32 v172, v36, v37
	v_lshlrev_b32_e32 v178, 16, v17
	v_and_b32_e32 v179, 0xffff0000, v17
	v_pk_add_f32 v[60:61], v[60:61], v[178:179] neg_lo:[0,1] neg_hi:[0,1]
	v_cvt_pk_bf16_f32 v173, v60, v61
	v_lshlrev_b32_e32 v176, 16, v18
	v_and_b32_e32 v177, 0xffff0000, v18
	v_pk_add_f32 v[38:39], v[38:39], v[176:177] neg_lo:[0,1] neg_hi:[0,1]
	v_cvt_pk_bf16_f32 v174, v38, v39
	v_lshlrev_b32_e32 v178, 16, v19
	v_and_b32_e32 v179, 0xffff0000, v19
	v_pk_add_f32 v[62:63], v[62:63], v[178:179] neg_lo:[0,1] neg_hi:[0,1]
	v_cvt_pk_bf16_f32 v175, v62, v63
	s_waitcnt vmcnt(10)
; #define RT_LOAD(fr, c) do { _Pragma("unroll") for (int i = 0; i < 16; ++i) fr[i] = WFRAG((c) * 16 + i); } while (0)
; template <int MODE>
; __device__ __forceinline__ void norm_phase(const MkArgs& a, LAS unsigned char* lds, const int l, const int wv) {
;     ...
;                 *(u32x4*)(hb + (size_t)t * DM + k) = o;
;     ...
;             RT_LOAD(frA, 0); RT_LOAD(frB, 1);
;             RT_MMA(frA, 0);
;             RT_LOAD(frA, 2);
;             RT_MMA(frB, 1);
;             RT_MMA(frA, 2);
;     ...
; #pragma unroll
;             for (int nt = 0; nt < 3; ++nt)
; #pragma unroll
;                 for (int e = 0; e < 4; ++e) part[(w * 16 + 4 * q + e) * 48 + 16 * nt + r] = acc[nt][e];
;     ...
;             __syncthreads();
	v_mfma_f32_16x16x32_bf16 v[160:163], v[16:19], v[242:245], v[160:163]
	v_mfma_f32_16x16x32_bf16 v[164:167], v[16:19], v[186:189], v[164:167]
	v_mfma_f32_16x16x32_bf16 v[168:171], v[16:19], v[194:197], v[168:171]
	v_mfma_f32_16x16x32_bf16 v[160:163], v[16:19], v[246:249], v[160:163]
	v_mfma_f32_16x16x32_bf16 v[164:167], v[16:19], v[190:193], v[164:167]
	v_mfma_f32_16x16x32_bf16 v[168:171], v[16:19], v[198:201], v[168:171]
	v_mfma_f32_16x16x32_bf16 v[160:163], v[172:175], v[242:245], v[160:163]
	v_mfma_f32_16x16x32_bf16 v[164:167], v[172:175], v[186:189], v[164:167]
	v_mfma_f32_16x16x32_bf16 v[168:171], v[172:175], v[194:197], v[168:171]
	global_load_dwordx4 v[242:245], v119, s[100:101] offset:2048
	global_load_dwordx4 v[246:249], v119, s[100:101] offset:3072
	v_lshlrev_b32_e32 v176, 16, v20
	v_and_b32_e32 v177, 0xffff0000, v20
	v_pk_add_f32 v[32:33], v[32:33], v[176:177] neg_lo:[0,1] neg_hi:[0,1]
	v_cvt_pk_bf16_f32 v172, v32, v33
	v_lshlrev_b32_e32 v178, 16, v21
	v_and_b32_e32 v179, 0xffff0000, v21
	v_pk_add_f32 v[82:83], v[82:83], v[178:179] neg_lo:[0,1] neg_hi:[0,1]
	v_cvt_pk_bf16_f32 v173, v82, v83
	v_lshlrev_b32_e32 v176, 16, v22
	v_and_b32_e32 v177, 0xffff0000, v22
	v_pk_add_f32 v[34:35], v[34:35], v[176:177] neg_lo:[0,1] neg_hi:[0,1]
	v_cvt_pk_bf16_f32 v174, v34, v35
	v_lshlrev_b32_e32 v178, 16, v23
	v_and_b32_e32 v179, 0xffff0000, v23
	v_pk_add_f32 v[84:85], v[84:85], v[178:179] neg_lo:[0,1] neg_hi:[0,1]
	v_cvt_pk_bf16_f32 v175, v84, v85
	s_waitcnt vmcnt(6)
	v_mfma_f32_16x16x32_bf16 v[160:163], v[20:23], v[202:205], v[160:163]
	v_mfma_f32_16x16x32_bf16 v[164:167], v[20:23], v[210:213], v[164:167]
	v_mfma_f32_16x16x32_bf16 v[168:171], v[20:23], v[218:221], v[168:171]
	v_mfma_f32_16x16x32_bf16 v[160:163], v[20:23], v[206:209], v[160:163]
	v_mfma_f32_16x16x32_bf16 v[164:167], v[20:23], v[214:217], v[164:167]
	v_mfma_f32_16x16x32_bf16 v[168:171], v[20:23], v[222:225], v[168:171]
	v_mfma_f32_16x16x32_bf16 v[160:163], v[172:175], v[202:205], v[160:163]
	v_mfma_f32_16x16x32_bf16 v[164:167], v[172:175], v[210:213], v[164:167]
	v_mfma_f32_16x16x32_bf16 v[168:171], v[172:175], v[218:221], v[168:171]
	v_lshlrev_b32_e32 v176, 16, v0
	v_and_b32_e32 v177, 0xffff0000, v0
	v_pk_add_f32 v[28:29], v[28:29], v[176:177] neg_lo:[0,1] neg_hi:[0,1]
	v_cvt_pk_bf16_f32 v172, v28, v29
	v_lshlrev_b32_e32 v178, 16, v1
	v_and_b32_e32 v179, 0xffff0000, v1
	v_pk_add_f32 v[86:87], v[86:87], v[178:179] neg_lo:[0,1] neg_hi:[0,1]
	v_cvt_pk_bf16_f32 v173, v86, v87
	v_lshlrev_b32_e32 v176, 16, v2
	v_and_b32_e32 v177, 0xffff0000, v2
	v_pk_add_f32 v[30:31], v[30:31], v[176:177] neg_lo:[0,1] neg_hi:[0,1]
	v_cvt_pk_bf16_f32 v174, v30, v31
	v_lshlrev_b32_e32 v178, 16, v3
	v_and_b32_e32 v179, 0xffff0000, v3
	v_pk_add_f32 v[88:89], v[88:89], v[178:179] neg_lo:[0,1] neg_hi:[0,1]
	v_cvt_pk_bf16_f32 v175, v88, v89
	s_waitcnt vmcnt(0)
	v_mfma_f32_16x16x32_bf16 v[160:163], v[0:3], v[226:229], v[160:163]
	v_mfma_f32_16x16x32_bf16 v[164:167], v[0:3], v[234:237], v[164:167]
	v_mfma_f32_16x16x32_bf16 v[168:171], v[0:3], v[242:245], v[168:171]
	v_mfma_f32_16x16x32_bf16 v[160:163], v[0:3], v[230:233], v[160:163]
	v_mfma_f32_16x16x32_bf16 v[164:167], v[0:3], v[238:241], v[164:167]
	v_mfma_f32_16x16x32_bf16 v[168:171], v[0:3], v[246:249], v[168:171]
	v_mfma_f32_16x16x32_bf16 v[160:163], v[172:175], v[226:229], v[160:163]
	v_mfma_f32_16x16x32_bf16 v[164:167], v[172:175], v[234:237], v[164:167]
	v_mfma_f32_16x16x32_bf16 v[168:171], v[172:175], v[242:245], v[168:171]
	global_store_dwordx4 v[250:251], v[44:47], off
	global_store_dwordx4 v[250:251], v[24:27], off offset:64
	global_store_dwordx4 v[250:251], v[4:7], off offset:128
	global_store_dwordx4 v[250:251], v[8:11], off offset:192
	global_store_dwordx4 v[250:251], v[12:15], off offset:256
	global_store_dwordx4 v[250:251], v[16:19], off offset:320
	global_store_dwordx4 v[250:251], v[20:23], off offset:384
	global_store_dwordx4 v[250:251], v[0:3], off offset:448
	v_add_u32_e32 v4, 0x400, v156
	s_nop 7
	s_nop 1
	ds_write2_b32 v4, v160, v164 offset1:16
	ds_write2_b32 v4, v162, v166 offset0:96 offset1:112
	ds_write2_b32 v4, v168, v161 offset0:32 offset1:48
	ds_write2_b32 v4, v165, v169 offset0:64 offset1:80
	ds_write2_b32 v4, v170, v163 offset0:128 offset1:144
	ds_write2_b32 v4, v167, v171 offset0:160 offset1:176
	s_waitcnt lgkmcnt(0)
	s_barrier
	s_and_saveexec_b64 s[12:13], s[6:7]
	s_cbranch_execz .LBB0_1976
	s_mov_b64 s[14:15], 0
	v_mov_b32_e32 v0, v114
	v_mov_b32_e32 v2, v64
